# hand-written register-only expert weight conversion (2 item pairs in flight) in SWA phase, both halves
# baseline (speedup 1.0000x reference)
; __device__ __forceinline__ unsigned cvt_pk4_fp8(float a, float b, float c, float d) { int w = 0; w = __builtin_amdgcn_cvt_pk_fp8_f32(a, b, w, false); w = __builtin_amdgcn_cvt_pk_fp8_f32(c, d, w, true); return (unsigned)w; }
; __device__ __forceinline__ void tr_item8(const float* W, int ld, int K, int nblk, int item, unsigned char* WT, bool gu, float scale, LAS float* scr, int lane) {
;     const int kb = item / nblk, nb = item % nblk, k0 = 64 * kb, n0 = 32 * nb;
;     int drow0 = n0;
;     if (gu) { const int bj = n0 / FF, j = n0 - bj * FF; drow0 = 256 * (j / 128) + 128 * bj + (j % 128); }
;     { float t_[32];
; #pragma unroll
;       for (int i = 0; i < 32; ++i) t_[i] = W[(size_t)(k0 + 2 * i + (lane >> 5)) * ld + n0 + (lane & 31)];
; #pragma unroll
;       for (int i = 0; i < 32; ++i) scr[(2 * i + (lane >> 5)) * 33 + (lane & 31)] = t_[i] * scale; }
;     LDS_WAIT(); asm volatile("" ::: "memory");
;     const int c = lane & 3;
; #pragma unroll
;     for (int j = 0; j < 2; ++j) { const int n = (lane >> 2) + 16 * j; const LAS float* sp = scr + (16 * c) * 33 + n;
;         v4u o; o.x = pg8::cvt_pk4_fp8(sp[0 * 33], sp[1 * 33], sp[2 * 33], sp[3 * 33]); o.y = pg8::cvt_pk4_fp8(sp[4 * 33], sp[5 * 33], sp[6 * 33], sp[7 * 33]);
;         o.z = pg8::cvt_pk4_fp8(sp[8 * 33], sp[9 * 33], sp[10 * 33], sp[11 * 33]); o.w = pg8::cvt_pk4_fp8(sp[12 * 33], sp[13 * 33], sp[14 * 33], sp[15 * 33]);
;         *(GAS v4u*)(WT + (size_t)(drow0 + n) * K + k0 + 16 * c) = o; }
; __global__ void __launch_bounds__(NWAVES * 64, 2) mk_fwd(Args args) {
;     ...
;         if (F.G == 256 && rep_ == 0) {
;             constexpr int NODD = CONV_SWA_ODD * 128 * NWAVES; const int lo = CONV_NITEMS - CONV_SWA;
;             const int rank = F.c >> 3, xcc = F.c & 7;
;             const bool att = F.loc ? (rank < 16) : ((F.c & 1) == 0);
;             const int half = F.loc ? (xcc * 16 + (rank & 15)) : (F.c >> 1), w = half * NWAVES + F.wave;
;             const int run = F.loc ? ((xcc >> 1) * 32 + (rank & 3) * 8 + (xcc & 1) * 4 + ((rank >> 2) & 3)) : half;
;             if (att) { swa_phase((char*)lds + RING_OFF, QO, KB, VB, XN, args.in[11], args.in[13], (LAS float*)(F.lds + RING_OFF + 100 * 1024), run, 128, F.wave);
;                        convert_items(F, args, lo + NODD, CONV_NITEMS, w, 128 * NWAVES); }
;             else convert_items(F, args, lo, lo + NODD, w, 128 * NWAVES); }
.LBB0_1325:
	s_and_b64 vcc, exec, s[0:1]
	s_cbranch_vccz .LBB0_1434
	s_ashr_i32 s4, s2, 3
	s_lshl_b32 s10, s2, 4
	s_and_b32 s0, s10, 0x70
	s_and_b32 s1, s4, 15
	v_readlane_b32 s6, v254, 24
	s_or_b32 s3, s0, s1
	s_ashr_i32 s11, s2, 1
	v_readlane_b32 s7, v254, 25
	s_and_b64 s[0:1], s[6:7], exec
	s_cselect_b32 s0, s11, s3
	s_lshl_b32 s3, s0, 3
	v_readlane_b32 s0, v254, 3
	s_add_i32 s3, s3, s0
	s_bitcmp0_b32 s2, 0
	s_cselect_b64 s[0:1], -1, 0
	s_cmp_lt_i32 s4, 16
	s_cselect_b64 s[4:5], -1, 0
	v_cndmask_b32_e64 v0, 0, 1, s[4:5]
	s_waitcnt lgkmcnt(0)
	v_cndmask_b32_e64 v1, 0, 1, s[0:1]
	v_cndmask_b32_e64 v0, v0, v1, s[6:7]
	v_and_b32_e32 v0, 1, v0
	v_cmp_eq_u32_e32 vcc, 0, v0
	s_mov_b64 s[0:1], -1
	s_cbranch_vccz .LBB0_1359
	s_cmpk_gt_i32 s3, 0x5fff
	v_mbcnt_lo_u32_b32 v4, -1, 0
	v_mbcnt_hi_u32_b32 v4, -1, v4
	s_cbranch_scc1 .LBB0_1358
	s_lshl_b32 s101, s3, 1
	s_add_u32 s101, s101, 0x5a00
	s_mov_b64 exec, -1
	v_readlane_b32 s0, v254, 32
	v_readlane_b32 s1, v254, 33
	v_readlane_b32 s4, v254, 34
	v_readlane_b32 s5, v254, 35
	s_add_u32 s6, s78, 0x2600000
	s_addc_u32 s7, s79, 0
	s_add_u32 s8, s78, 0x5e00000
	s_addc_u32 s9, s79, 0
	s_movk_i32 s100, 12
	v_mbcnt_lo_u32_b32 v170, -1, 0
	v_mbcnt_hi_u32_b32 v170, -1, v170
	v_and_b32_e32 v171, 31, v170
	v_lshrrev_b32_e32 v172, 5, v170
	v_lshlrev_b32_e32 v170, 3, v171
	s_mov_b32 s55, 0xe0000
	v_mul_lo_u32 v166, v172, s55
	v_add_u32_e32 v166, v166, v170
	v_lshlrev_b32_e32 v167, 17, v172
	v_add_u32_e32 v167, v167, v170
	v_lshlrev_b32_e32 v172, 5, v172
	v_lshl_add_u32 v168, v171, 11, v172
	s_movk_i32 s55, 0x1c00
	v_mul_lo_u32 v169, v171, s55
	v_add_u32_e32 v169, v169, v172
	s_sub_u32 s55, s101, 0x2200
	s_cmp_lt_u32 s55, 0x7000
	s_cbranch_scc0 .LfcA_dn_p0
	s_lshr_b32 s54, s55, 9
	s_mulk_i32 s54, 0x2493
	s_lshr_b32 s54, s54, 16
	s_mul_i32 s53, s54, 0xe00
	s_sub_u32 s53, s55, s53
	s_lshr_b32 s52, s53, 5
	s_mulk_i32 s52, 0x2493
	s_lshr_b32 s52, s52, 16
	s_mul_i32 s51, s52, 0xe0
	s_sub_u32 s51, s53, s51
	s_mul_i32 s50, s54, 0x1c00000
	s_mul_i32 s49, s52, 0x1c0000
	s_add_u32 s50, s50, s49
	s_lshl_b32 s49, s51, 7
	s_add_u32 s50, s50, s49
	s_add_u32 s12, s0, s50
	s_addc_u32 s13, s1, 0
	s_cmp_ge_u32 s51, 0x70
	s_cselect_b32 s50, 1, 0
	s_mul_i32 s49, s50, 0x70
	s_sub_u32 s49, s51, s49
	s_lshr_b32 s48, s49, 2
	s_lshl_b32 s48, s48, 8
	s_lshl_b32 s50, s50, 7
	s_add_u32 s48, s48, s50
	s_and_b32 s49, s49, 3
	s_lshl_b32 s49, s49, 5
	s_add_u32 s48, s48, s49
	s_lshl_b32 s48, s48, 10
	s_mul_i32 s50, s54, 0x700000
	s_add_u32 s48, s48, s50
	s_lshl_b32 s50, s52, 6
	s_add_u32 s48, s48, s50
	s_add_u32 s14, s6, s48
	s_addc_u32 s15, s7, 0
	s_movk_i32 s99, 0x7000
	s_mov_b32 s16, 0x42800000
	v_mov_b32_e32 v160, v166
	v_mov_b32_e32 v162, v168
	v_add_u32_e32 v164, 0x400, v168
	s_branch .LfcA_set_p0
.LfcA_dn_p0:
	s_sub_u32 s55, s55, 0x7000
	s_lshr_b32 s54, s55, 8
	s_mulk_i32 s54, 0x2493
	s_lshr_b32 s54, s54, 16
	s_mul_i32 s53, s54, 0x700
	s_sub_u32 s53, s55, s53
	s_lshr_b32 s52, s53, 5
	s_and_b32 s51, s53, 31
	s_mul_i32 s50, s54, 0xe00000
	s_lshl_b32 s49, s52, 18
	s_add_u32 s50, s50, s49
	s_lshl_b32 s49, s51, 7
	s_add_u32 s50, s50, s49
	s_add_u32 s12, s4, s50
	s_addc_u32 s13, s5, 0
	s_mul_i32 s50, s54, 0x380000
	s_mul_i32 s49, s51, 0x1c000
	s_add_u32 s50, s50, s49
	s_lshl_b32 s49, s52, 6
	s_add_u32 s50, s50, s49
	s_add_u32 s14, s8, s50
	s_addc_u32 s15, s9, 0
	s_movk_i32 s99, 0x1000
	s_mov_b32 s16, 0x43000000
	v_mov_b32_e32 v160, v167
	v_mov_b32_e32 v162, v169
	v_add_u32_e32 v164, 0xe00, v169
.LfcA_set_p0:
	s_add_u32 s101, s101, 0x800
	s_mov_b64 s[44:45], s[12:13]
	global_load_dwordx2 v[0:1], v160, s[44:45]
	s_add_u32 s44, s44, s99
	s_addc_u32 s45, s45, 0
	global_load_dwordx2 v[2:3], v160, s[44:45]
	s_add_u32 s44, s44, s99
	s_addc_u32 s45, s45, 0
	global_load_dwordx2 v[4:5], v160, s[44:45]
	s_add_u32 s44, s44, s99
	s_addc_u32 s45, s45, 0
	global_load_dwordx2 v[6:7], v160, s[44:45]
	s_add_u32 s44, s44, s99
	s_addc_u32 s45, s45, 0
	global_load_dwordx2 v[8:9], v160, s[44:45]
	s_add_u32 s44, s44, s99
	s_addc_u32 s45, s45, 0
	global_load_dwordx2 v[10:11], v160, s[44:45]
	s_add_u32 s44, s44, s99
	s_addc_u32 s45, s45, 0
	global_load_dwordx2 v[12:13], v160, s[44:45]
	s_add_u32 s44, s44, s99
	s_addc_u32 s45, s45, 0
	global_load_dwordx2 v[14:15], v160, s[44:45]
	s_add_u32 s44, s44, s99
	s_addc_u32 s45, s45, 0
	global_load_dwordx2 v[16:17], v160, s[44:45]
	s_add_u32 s44, s44, s99
	s_addc_u32 s45, s45, 0
	global_load_dwordx2 v[18:19], v160, s[44:45]
	s_add_u32 s44, s44, s99
	s_addc_u32 s45, s45, 0
	global_load_dwordx2 v[20:21], v160, s[44:45]
	s_add_u32 s44, s44, s99
	s_addc_u32 s45, s45, 0
	global_load_dwordx2 v[22:23], v160, s[44:45]
	s_add_u32 s44, s44, s99
	s_addc_u32 s45, s45, 0
	global_load_dwordx2 v[24:25], v160, s[44:45]
	s_add_u32 s44, s44, s99
	s_addc_u32 s45, s45, 0
	global_load_dwordx2 v[26:27], v160, s[44:45]
	s_add_u32 s44, s44, s99
	s_addc_u32 s45, s45, 0
	global_load_dwordx2 v[28:29], v160, s[44:45]
	s_add_u32 s44, s44, s99
	s_addc_u32 s45, s45, 0
	global_load_dwordx2 v[30:31], v160, s[44:45]
	s_add_u32 s44, s44, s99
	s_addc_u32 s45, s45, 0
	global_load_dwordx2 v[32:33], v160, s[44:45]
	s_add_u32 s44, s44, s99
	s_addc_u32 s45, s45, 0
	global_load_dwordx2 v[34:35], v160, s[44:45]
	s_add_u32 s44, s44, s99
	s_addc_u32 s45, s45, 0
	global_load_dwordx2 v[36:37], v160, s[44:45]
	s_add_u32 s44, s44, s99
	s_addc_u32 s45, s45, 0
	global_load_dwordx2 v[38:39], v160, s[44:45]
	s_add_u32 s44, s44, s99
	s_addc_u32 s45, s45, 0
	global_load_dwordx2 v[40:41], v160, s[44:45]
	s_add_u32 s44, s44, s99
	s_addc_u32 s45, s45, 0
	global_load_dwordx2 v[42:43], v160, s[44:45]
	s_add_u32 s44, s44, s99
	s_addc_u32 s45, s45, 0
	global_load_dwordx2 v[44:45], v160, s[44:45]
	s_add_u32 s44, s44, s99
	s_addc_u32 s45, s45, 0
	global_load_dwordx2 v[46:47], v160, s[44:45]
	s_add_u32 s44, s44, s99
	s_addc_u32 s45, s45, 0
	global_load_dwordx2 v[48:49], v160, s[44:45]
	s_add_u32 s44, s44, s99
	s_addc_u32 s45, s45, 0
	global_load_dwordx2 v[50:51], v160, s[44:45]
	s_add_u32 s44, s44, s99
	s_addc_u32 s45, s45, 0
	global_load_dwordx2 v[52:53], v160, s[44:45]
	s_add_u32 s44, s44, s99
	s_addc_u32 s45, s45, 0
	global_load_dwordx2 v[54:55], v160, s[44:45]
	s_add_u32 s44, s44, s99
	s_addc_u32 s45, s45, 0
	global_load_dwordx2 v[56:57], v160, s[44:45]
	s_add_u32 s44, s44, s99
	s_addc_u32 s45, s45, 0
	global_load_dwordx2 v[58:59], v160, s[44:45]
	s_add_u32 s44, s44, s99
	s_addc_u32 s45, s45, 0
	global_load_dwordx2 v[60:61], v160, s[44:45]
	s_add_u32 s44, s44, s99
	s_addc_u32 s45, s45, 0
	global_load_dwordx2 v[62:63], v160, s[44:45]
	s_sub_u32 s55, s101, 0x2200
	s_cmp_lt_u32 s55, 0x7000
	s_cbranch_scc0 .LfcA_dn_p1
; __device__ __forceinline__ void tr_item8(const float* W, int ld, int K, int nblk, int item, unsigned char* WT, bool gu, float scale, LAS float* scr, int lane) {
;     const int kb = item / nblk, nb = item % nblk, k0 = 64 * kb, n0 = 32 * nb;
;     int drow0 = n0;
;     if (gu) { const int bj = n0 / FF, j = n0 - bj * FF; drow0 = 256 * (j / 128) + 128 * bj + (j % 128); }
;     { float t_[32];
; #pragma unroll
;       for (int i = 0; i < 32; ++i) t_[i] = W[(size_t)(k0 + 2 * i + (lane >> 5)) * ld + n0 + (lane & 31)];
; #pragma unroll
;       for (int i = 0; i < 32; ++i) scr[(2 * i + (lane >> 5)) * 33 + (lane & 31)] = t_[i] * scale; }
; __device__ __forceinline__ void convert_items(Frame& F, const Args& a, int lo, int hi, int w, int nw) {
;     ...
;         if (r < NE * I_GU) { const int e = r / I_GU, rr = r % I_GU; tr_item8(a.in[18] + (size_t)e * D * 2 * FF, 2 * FF, D, 224, rr, F.ws + WS_WMGU + (size_t)e * 2 * FF * D, true, WSC_GU, scr, lane); continue; } r -= NE * I_GU;
;         { const int e = r / I_DN, rr = r % I_DN; tr_item8(a.in[19] + (size_t)e * FF * D, D, FF, 32, rr, F.ws + WS_WMDN + (size_t)e * D * FF, false, WSC_DN, scr, lane); }
	s_lshr_b32 s54, s55, 9
	s_mulk_i32 s54, 0x2493
	s_lshr_b32 s54, s54, 16
	s_mul_i32 s53, s54, 0xe00
	s_sub_u32 s53, s55, s53
	s_lshr_b32 s52, s53, 5
	s_mulk_i32 s52, 0x2493
	s_lshr_b32 s52, s52, 16
	s_mul_i32 s51, s52, 0xe0
	s_sub_u32 s51, s53, s51
	s_mul_i32 s50, s54, 0x1c00000
	s_mul_i32 s49, s52, 0x1c0000
	s_add_u32 s50, s50, s49
	s_lshl_b32 s49, s51, 7
	s_add_u32 s50, s50, s49
	s_add_u32 s30, s0, s50
	s_addc_u32 s31, s1, 0
	s_cmp_ge_u32 s51, 0x70
	s_cselect_b32 s50, 1, 0
	s_mul_i32 s49, s50, 0x70
	s_sub_u32 s49, s51, s49
	s_lshr_b32 s48, s49, 2
	s_lshl_b32 s48, s48, 8
	s_lshl_b32 s50, s50, 7
	s_add_u32 s48, s48, s50
	s_and_b32 s49, s49, 3
	s_lshl_b32 s49, s49, 5
	s_add_u32 s48, s48, s49
	s_lshl_b32 s48, s48, 10
	s_mul_i32 s50, s54, 0x700000
	s_add_u32 s48, s48, s50
	s_lshl_b32 s50, s52, 6
	s_add_u32 s48, s48, s50
	s_add_u32 s40, s6, s48
	s_addc_u32 s41, s7, 0
	s_movk_i32 s98, 0x7000
	s_mov_b32 s42, 0x42800000
	v_mov_b32_e32 v161, v166
	v_mov_b32_e32 v163, v168
	v_add_u32_e32 v165, 0x400, v168
	s_branch .LfcA_set_p1
.LfcA_dn_p1:
	s_sub_u32 s55, s55, 0x7000
	s_lshr_b32 s54, s55, 8
	s_mulk_i32 s54, 0x2493
	s_lshr_b32 s54, s54, 16
	s_mul_i32 s53, s54, 0x700
	s_sub_u32 s53, s55, s53
	s_lshr_b32 s52, s53, 5
	s_and_b32 s51, s53, 31
	s_mul_i32 s50, s54, 0xe00000
	s_lshl_b32 s49, s52, 18
	s_add_u32 s50, s50, s49
	s_lshl_b32 s49, s51, 7
	s_add_u32 s50, s50, s49
	s_add_u32 s30, s4, s50
	s_addc_u32 s31, s5, 0
	s_mul_i32 s50, s54, 0x380000
	s_mul_i32 s49, s51, 0x1c000
	s_add_u32 s50, s50, s49
	s_lshl_b32 s49, s52, 6
	s_add_u32 s50, s50, s49
	s_add_u32 s40, s8, s50
	s_addc_u32 s41, s9, 0
	s_movk_i32 s98, 0x1000
	s_mov_b32 s42, 0x43000000
	v_mov_b32_e32 v161, v167
	v_mov_b32_e32 v163, v169
	v_add_u32_e32 v165, 0xe00, v169
.LfcA_set_p1:
	s_add_u32 s101, s101, 0x800
	s_mov_b64 s[44:45], s[30:31]
	global_load_dwordx2 v[64:65], v161, s[44:45]
	s_add_u32 s44, s44, s98
	s_addc_u32 s45, s45, 0
	global_load_dwordx2 v[66:67], v161, s[44:45]
	s_add_u32 s44, s44, s98
	s_addc_u32 s45, s45, 0
	global_load_dwordx2 v[68:69], v161, s[44:45]
	s_add_u32 s44, s44, s98
	s_addc_u32 s45, s45, 0
	global_load_dwordx2 v[70:71], v161, s[44:45]
	s_add_u32 s44, s44, s98
	s_addc_u32 s45, s45, 0
	global_load_dwordx2 v[72:73], v161, s[44:45]
	s_add_u32 s44, s44, s98
	s_addc_u32 s45, s45, 0
	global_load_dwordx2 v[74:75], v161, s[44:45]
	s_add_u32 s44, s44, s98
	s_addc_u32 s45, s45, 0
	global_load_dwordx2 v[76:77], v161, s[44:45]
	s_add_u32 s44, s44, s98
	s_addc_u32 s45, s45, 0
	global_load_dwordx2 v[78:79], v161, s[44:45]
	s_add_u32 s44, s44, s98
	s_addc_u32 s45, s45, 0
	global_load_dwordx2 v[80:81], v161, s[44:45]
	s_add_u32 s44, s44, s98
	s_addc_u32 s45, s45, 0
	global_load_dwordx2 v[82:83], v161, s[44:45]
	s_add_u32 s44, s44, s98
	s_addc_u32 s45, s45, 0
	global_load_dwordx2 v[84:85], v161, s[44:45]
	s_add_u32 s44, s44, s98
	s_addc_u32 s45, s45, 0
	global_load_dwordx2 v[86:87], v161, s[44:45]
	s_add_u32 s44, s44, s98
	s_addc_u32 s45, s45, 0
	global_load_dwordx2 v[88:89], v161, s[44:45]
	s_add_u32 s44, s44, s98
	s_addc_u32 s45, s45, 0
	global_load_dwordx2 v[90:91], v161, s[44:45]
	s_add_u32 s44, s44, s98
	s_addc_u32 s45, s45, 0
	global_load_dwordx2 v[92:93], v161, s[44:45]
	s_add_u32 s44, s44, s98
	s_addc_u32 s45, s45, 0
	global_load_dwordx2 v[94:95], v161, s[44:45]
	s_add_u32 s44, s44, s98
	s_addc_u32 s45, s45, 0
	global_load_dwordx2 v[96:97], v161, s[44:45]
	s_add_u32 s44, s44, s98
	s_addc_u32 s45, s45, 0
	global_load_dwordx2 v[98:99], v161, s[44:45]
	s_add_u32 s44, s44, s98
	s_addc_u32 s45, s45, 0
	global_load_dwordx2 v[100:101], v161, s[44:45]
	s_add_u32 s44, s44, s98
	s_addc_u32 s45, s45, 0
	global_load_dwordx2 v[102:103], v161, s[44:45]
	s_add_u32 s44, s44, s98
	s_addc_u32 s45, s45, 0
	global_load_dwordx2 v[104:105], v161, s[44:45]
	s_add_u32 s44, s44, s98
	s_addc_u32 s45, s45, 0
	global_load_dwordx2 v[106:107], v161, s[44:45]
	s_add_u32 s44, s44, s98
	s_addc_u32 s45, s45, 0
	global_load_dwordx2 v[108:109], v161, s[44:45]
	s_add_u32 s44, s44, s98
	s_addc_u32 s45, s45, 0
	global_load_dwordx2 v[110:111], v161, s[44:45]
	s_add_u32 s44, s44, s98
	s_addc_u32 s45, s45, 0
	global_load_dwordx2 v[112:113], v161, s[44:45]
	s_add_u32 s44, s44, s98
	s_addc_u32 s45, s45, 0
	global_load_dwordx2 v[114:115], v161, s[44:45]
	s_add_u32 s44, s44, s98
	s_addc_u32 s45, s45, 0
	global_load_dwordx2 v[116:117], v161, s[44:45]
	s_add_u32 s44, s44, s98
	s_addc_u32 s45, s45, 0
	global_load_dwordx2 v[118:119], v161, s[44:45]
	s_add_u32 s44, s44, s98
	s_addc_u32 s45, s45, 0
	global_load_dwordx2 v[120:121], v161, s[44:45]
	s_add_u32 s44, s44, s98
	s_addc_u32 s45, s45, 0
	global_load_dwordx2 v[122:123], v161, s[44:45]
	s_add_u32 s44, s44, s98
	s_addc_u32 s45, s45, 0
	global_load_dwordx2 v[124:125], v161, s[44:45]
	s_add_u32 s44, s44, s98
	s_addc_u32 s45, s45, 0
	global_load_dwordx2 v[126:127], v161, s[44:45]
	s_cmp_le_u32 s100, 2
	s_cbranch_scc1 .LfcA_epi
; __device__ __forceinline__ unsigned cvt_pk4_fp8(float a, float b, float c, float d) { int w = 0; w = __builtin_amdgcn_cvt_pk_fp8_f32(a, b, w, false); w = __builtin_amdgcn_cvt_pk_fp8_f32(c, d, w, true); return (unsigned)w; }
; #define GAS __attribute__((address_space(1)))
; #define LAS __attribute__((address_space(3)))
; #define LDS_WAIT() asm volatile("s_waitcnt lgkmcnt(0)" ::: "memory")
; __device__ __forceinline__ void tr_item8(const float* W, int ld, int K, int nblk, int item, unsigned char* WT, bool gu, float scale, LAS float* scr, int lane) {
;     ...
; #pragma unroll
;       for (int i = 0; i < 32; ++i) t_[i] = W[(size_t)(k0 + 2 * i + (lane >> 5)) * ld + n0 + (lane & 31)];
; #pragma unroll
;       for (int i = 0; i < 32; ++i) scr[(2 * i + (lane >> 5)) * 33 + (lane & 31)] = t_[i] * scale; }
;     LDS_WAIT(); asm volatile("" ::: "memory");
;     const int c = lane & 3;
; #pragma unroll
;     for (int j = 0; j < 2; ++j) { const int n = (lane >> 2) + 16 * j; const LAS float* sp = scr + (16 * c) * 33 + n;
;         v4u o; o.x = pg8::cvt_pk4_fp8(sp[0 * 33], sp[1 * 33], sp[2 * 33], sp[3 * 33]); o.y = pg8::cvt_pk4_fp8(sp[4 * 33], sp[5 * 33], sp[6 * 33], sp[7 * 33]);
;         o.z = pg8::cvt_pk4_fp8(sp[8 * 33], sp[9 * 33], sp[10 * 33], sp[11 * 33]); o.w = pg8::cvt_pk4_fp8(sp[12 * 33], sp[13 * 33], sp[14 * 33], sp[15 * 33]);
;         *(GAS v4u*)(WT + (size_t)(drow0 + n) * K + k0 + 16 * c) = o; }
.LfcA_loop:
	s_waitcnt vmcnt(32)
	v_pk_mul_f32 v[0:1], v[0:1], s[16:17] op_sel_hi:[1,0]
	v_pk_mul_f32 v[2:3], v[2:3], s[16:17] op_sel_hi:[1,0]
	v_pk_mul_f32 v[4:5], v[4:5], s[16:17] op_sel_hi:[1,0]
	v_pk_mul_f32 v[6:7], v[6:7], s[16:17] op_sel_hi:[1,0]
	v_pk_mul_f32 v[8:9], v[8:9], s[16:17] op_sel_hi:[1,0]
	v_pk_mul_f32 v[10:11], v[10:11], s[16:17] op_sel_hi:[1,0]
	v_pk_mul_f32 v[12:13], v[12:13], s[16:17] op_sel_hi:[1,0]
	v_pk_mul_f32 v[14:15], v[14:15], s[16:17] op_sel_hi:[1,0]
	v_pk_mul_f32 v[16:17], v[16:17], s[16:17] op_sel_hi:[1,0]
	v_pk_mul_f32 v[18:19], v[18:19], s[16:17] op_sel_hi:[1,0]
	v_pk_mul_f32 v[20:21], v[20:21], s[16:17] op_sel_hi:[1,0]
	v_pk_mul_f32 v[22:23], v[22:23], s[16:17] op_sel_hi:[1,0]
	v_pk_mul_f32 v[24:25], v[24:25], s[16:17] op_sel_hi:[1,0]
	v_pk_mul_f32 v[26:27], v[26:27], s[16:17] op_sel_hi:[1,0]
	v_pk_mul_f32 v[28:29], v[28:29], s[16:17] op_sel_hi:[1,0]
	v_pk_mul_f32 v[30:31], v[30:31], s[16:17] op_sel_hi:[1,0]
	v_pk_mul_f32 v[32:33], v[32:33], s[16:17] op_sel_hi:[1,0]
	v_pk_mul_f32 v[34:35], v[34:35], s[16:17] op_sel_hi:[1,0]
	v_pk_mul_f32 v[36:37], v[36:37], s[16:17] op_sel_hi:[1,0]
	v_pk_mul_f32 v[38:39], v[38:39], s[16:17] op_sel_hi:[1,0]
	v_pk_mul_f32 v[40:41], v[40:41], s[16:17] op_sel_hi:[1,0]
	v_pk_mul_f32 v[42:43], v[42:43], s[16:17] op_sel_hi:[1,0]
	v_pk_mul_f32 v[44:45], v[44:45], s[16:17] op_sel_hi:[1,0]
	v_pk_mul_f32 v[46:47], v[46:47], s[16:17] op_sel_hi:[1,0]
	v_pk_mul_f32 v[48:49], v[48:49], s[16:17] op_sel_hi:[1,0]
	v_pk_mul_f32 v[50:51], v[50:51], s[16:17] op_sel_hi:[1,0]
	v_pk_mul_f32 v[52:53], v[52:53], s[16:17] op_sel_hi:[1,0]
	v_pk_mul_f32 v[54:55], v[54:55], s[16:17] op_sel_hi:[1,0]
	v_pk_mul_f32 v[56:57], v[56:57], s[16:17] op_sel_hi:[1,0]
	v_pk_mul_f32 v[58:59], v[58:59], s[16:17] op_sel_hi:[1,0]
	v_pk_mul_f32 v[60:61], v[60:61], s[16:17] op_sel_hi:[1,0]
	v_pk_mul_f32 v[62:63], v[62:63], s[16:17] op_sel_hi:[1,0]
	v_cvt_pk_fp8_f32 v128, v0, v2
	v_cvt_pk_fp8_f32 v129, v8, v10
	v_cvt_pk_fp8_f32 v130, v16, v18
	v_cvt_pk_fp8_f32 v131, v24, v26
	v_cvt_pk_fp8_f32 v132, v32, v34
	v_cvt_pk_fp8_f32 v133, v40, v42
	v_cvt_pk_fp8_f32 v134, v48, v50
	v_cvt_pk_fp8_f32 v135, v56, v58
	v_cvt_pk_fp8_f32 v128, v4, v6 op_sel:[0,0,1]
	v_cvt_pk_fp8_f32 v129, v12, v14 op_sel:[0,0,1]
	v_cvt_pk_fp8_f32 v130, v20, v22 op_sel:[0,0,1]
	v_cvt_pk_fp8_f32 v131, v28, v30 op_sel:[0,0,1]
	v_cvt_pk_fp8_f32 v132, v36, v38 op_sel:[0,0,1]
	v_cvt_pk_fp8_f32 v133, v44, v46 op_sel:[0,0,1]
	v_cvt_pk_fp8_f32 v134, v52, v54 op_sel:[0,0,1]
	v_cvt_pk_fp8_f32 v135, v60, v62 op_sel:[0,0,1]
	v_cvt_pk_fp8_f32 v136, v1, v3
	v_cvt_pk_fp8_f32 v137, v9, v11
	v_cvt_pk_fp8_f32 v138, v17, v19
	v_cvt_pk_fp8_f32 v139, v25, v27
	v_cvt_pk_fp8_f32 v140, v33, v35
	v_cvt_pk_fp8_f32 v141, v41, v43
	v_cvt_pk_fp8_f32 v142, v49, v51
	v_cvt_pk_fp8_f32 v143, v57, v59
	v_cvt_pk_fp8_f32 v136, v5, v7 op_sel:[0,0,1]
	v_cvt_pk_fp8_f32 v137, v13, v15 op_sel:[0,0,1]
	v_cvt_pk_fp8_f32 v138, v21, v23 op_sel:[0,0,1]
	v_cvt_pk_fp8_f32 v139, v29, v31 op_sel:[0,0,1]
	v_cvt_pk_fp8_f32 v140, v37, v39 op_sel:[0,0,1]
	v_cvt_pk_fp8_f32 v141, v45, v47 op_sel:[0,0,1]
	v_cvt_pk_fp8_f32 v142, v53, v55 op_sel:[0,0,1]
	v_cvt_pk_fp8_f32 v143, v61, v63 op_sel:[0,0,1]
	s_nop 1
	global_store_dwordx4 v162, v[128:131], s[14:15]
	global_store_dwordx4 v162, v[132:135], s[14:15] offset:16
	global_store_dwordx4 v164, v[136:139], s[14:15]
	global_store_dwordx4 v164, v[140:143], s[14:15] offset:16
	s_sub_u32 s55, s101, 0x2200
	s_cmp_lt_u32 s55, 0x7000
	s_cbranch_scc0 .LfcA_dn_l0
	s_lshr_b32 s54, s55, 9
	s_mulk_i32 s54, 0x2493
	s_lshr_b32 s54, s54, 16
	s_mul_i32 s53, s54, 0xe00
	s_sub_u32 s53, s55, s53
	s_lshr_b32 s52, s53, 5
	s_mulk_i32 s52, 0x2493
	s_lshr_b32 s52, s52, 16
	s_mul_i32 s51, s52, 0xe0
	s_sub_u32 s51, s53, s51
	s_mul_i32 s50, s54, 0x1c00000
	s_mul_i32 s49, s52, 0x1c0000
	s_add_u32 s50, s50, s49
	s_lshl_b32 s49, s51, 7
	s_add_u32 s50, s50, s49
	s_add_u32 s12, s0, s50
	s_addc_u32 s13, s1, 0
	s_cmp_ge_u32 s51, 0x70
	s_cselect_b32 s50, 1, 0
	s_mul_i32 s49, s50, 0x70
	s_sub_u32 s49, s51, s49
	s_lshr_b32 s48, s49, 2
	s_lshl_b32 s48, s48, 8
	s_lshl_b32 s50, s50, 7
	s_add_u32 s48, s48, s50
	s_and_b32 s49, s49, 3
	s_lshl_b32 s49, s49, 5
	s_add_u32 s48, s48, s49
	s_lshl_b32 s48, s48, 10
	s_mul_i32 s50, s54, 0x700000
	s_add_u32 s48, s48, s50
	s_lshl_b32 s50, s52, 6
	s_add_u32 s48, s48, s50
	s_add_u32 s14, s6, s48
	s_addc_u32 s15, s7, 0
	s_movk_i32 s99, 0x7000
	s_mov_b32 s16, 0x42800000
	v_mov_b32_e32 v160, v166
	v_mov_b32_e32 v162, v168
	v_add_u32_e32 v164, 0x400, v168
	s_branch .LfcA_set_l0

; __device__ __forceinline__ unsigned cvt_pk4_fp8(float a, float b, float c, float d) { int w = 0; w = __builtin_amdgcn_cvt_pk_fp8_f32(a, b, w, false); w = __builtin_amdgcn_cvt_pk_fp8_f32(c, d, w, true); return (unsigned)w; }
; #define GAS __attribute__((address_space(1)))
; #define LAS __attribute__((address_space(3)))
; #define LDS_WAIT() asm volatile("s_waitcnt lgkmcnt(0)" ::: "memory")
; __device__ __forceinline__ void tr_item8(const float* W, int ld, int K, int nblk, int item, unsigned char* WT, bool gu, float scale, LAS float* scr, int lane) {
;     ...
;     { float t_[32];
; #pragma unroll
;       for (int i = 0; i < 32; ++i) t_[i] = W[(size_t)(k0 + 2 * i + (lane >> 5)) * ld + n0 + (lane & 31)];
; #pragma unroll
;       for (int i = 0; i < 32; ++i) scr[(2 * i + (lane >> 5)) * 33 + (lane & 31)] = t_[i] * scale; }
;     LDS_WAIT(); asm volatile("" ::: "memory");
;     const int c = lane & 3;
; #pragma unroll
;     for (int j = 0; j < 2; ++j) { const int n = (lane >> 2) + 16 * j; const LAS float* sp = scr + (16 * c) * 33 + n;
;         v4u o; o.x = pg8::cvt_pk4_fp8(sp[0 * 33], sp[1 * 33], sp[2 * 33], sp[3 * 33]); o.y = pg8::cvt_pk4_fp8(sp[4 * 33], sp[5 * 33], sp[6 * 33], sp[7 * 33]);
;         o.z = pg8::cvt_pk4_fp8(sp[8 * 33], sp[9 * 33], sp[10 * 33], sp[11 * 33]); o.w = pg8::cvt_pk4_fp8(sp[12 * 33], sp[13 * 33], sp[14 * 33], sp[15 * 33]);
;         *(GAS v4u*)(WT + (size_t)(drow0 + n) * K + k0 + 16 * c) = o; }
.LfcA_set_l0:
	s_add_u32 s101, s101, 0x800
	s_mov_b64 s[44:45], s[12:13]
	global_load_dwordx2 v[0:1], v160, s[44:45]
	s_add_u32 s44, s44, s99
	s_addc_u32 s45, s45, 0
	global_load_dwordx2 v[2:3], v160, s[44:45]
	s_add_u32 s44, s44, s99
	s_addc_u32 s45, s45, 0
	global_load_dwordx2 v[4:5], v160, s[44:45]
	s_add_u32 s44, s44, s99
	s_addc_u32 s45, s45, 0
	global_load_dwordx2 v[6:7], v160, s[44:45]
	s_add_u32 s44, s44, s99
	s_addc_u32 s45, s45, 0
	global_load_dwordx2 v[8:9], v160, s[44:45]
	s_add_u32 s44, s44, s99
	s_addc_u32 s45, s45, 0
	global_load_dwordx2 v[10:11], v160, s[44:45]
	s_add_u32 s44, s44, s99
	s_addc_u32 s45, s45, 0
	global_load_dwordx2 v[12:13], v160, s[44:45]
	s_add_u32 s44, s44, s99
	s_addc_u32 s45, s45, 0
	global_load_dwordx2 v[14:15], v160, s[44:45]
	s_add_u32 s44, s44, s99
	s_addc_u32 s45, s45, 0
	global_load_dwordx2 v[16:17], v160, s[44:45]
	s_add_u32 s44, s44, s99
	s_addc_u32 s45, s45, 0
	global_load_dwordx2 v[18:19], v160, s[44:45]
	s_add_u32 s44, s44, s99
	s_addc_u32 s45, s45, 0
	global_load_dwordx2 v[20:21], v160, s[44:45]
	s_add_u32 s44, s44, s99
	s_addc_u32 s45, s45, 0
	global_load_dwordx2 v[22:23], v160, s[44:45]
	s_add_u32 s44, s44, s99
	s_addc_u32 s45, s45, 0
	global_load_dwordx2 v[24:25], v160, s[44:45]
	s_add_u32 s44, s44, s99
	s_addc_u32 s45, s45, 0
	global_load_dwordx2 v[26:27], v160, s[44:45]
	s_add_u32 s44, s44, s99
	s_addc_u32 s45, s45, 0
	global_load_dwordx2 v[28:29], v160, s[44:45]
	s_add_u32 s44, s44, s99
	s_addc_u32 s45, s45, 0
	global_load_dwordx2 v[30:31], v160, s[44:45]
	s_add_u32 s44, s44, s99
	s_addc_u32 s45, s45, 0
	global_load_dwordx2 v[32:33], v160, s[44:45]
	s_add_u32 s44, s44, s99
	s_addc_u32 s45, s45, 0
	global_load_dwordx2 v[34:35], v160, s[44:45]
	s_add_u32 s44, s44, s99
	s_addc_u32 s45, s45, 0
	global_load_dwordx2 v[36:37], v160, s[44:45]
	s_add_u32 s44, s44, s99
	s_addc_u32 s45, s45, 0
	global_load_dwordx2 v[38:39], v160, s[44:45]
	s_add_u32 s44, s44, s99
	s_addc_u32 s45, s45, 0
	global_load_dwordx2 v[40:41], v160, s[44:45]
	s_add_u32 s44, s44, s99
	s_addc_u32 s45, s45, 0
	global_load_dwordx2 v[42:43], v160, s[44:45]
	s_add_u32 s44, s44, s99
	s_addc_u32 s45, s45, 0
	global_load_dwordx2 v[44:45], v160, s[44:45]
	s_add_u32 s44, s44, s99
	s_addc_u32 s45, s45, 0
	global_load_dwordx2 v[46:47], v160, s[44:45]
	s_add_u32 s44, s44, s99
	s_addc_u32 s45, s45, 0
	global_load_dwordx2 v[48:49], v160, s[44:45]
	s_add_u32 s44, s44, s99
	s_addc_u32 s45, s45, 0
	global_load_dwordx2 v[50:51], v160, s[44:45]
	s_add_u32 s44, s44, s99
	s_addc_u32 s45, s45, 0
	global_load_dwordx2 v[52:53], v160, s[44:45]
	s_add_u32 s44, s44, s99
	s_addc_u32 s45, s45, 0
	global_load_dwordx2 v[54:55], v160, s[44:45]
	s_add_u32 s44, s44, s99
	s_addc_u32 s45, s45, 0
	global_load_dwordx2 v[56:57], v160, s[44:45]
	s_add_u32 s44, s44, s99
	s_addc_u32 s45, s45, 0
	global_load_dwordx2 v[58:59], v160, s[44:45]
	s_add_u32 s44, s44, s99
	s_addc_u32 s45, s45, 0
	global_load_dwordx2 v[60:61], v160, s[44:45]
	s_add_u32 s44, s44, s99
	s_addc_u32 s45, s45, 0
	global_load_dwordx2 v[62:63], v160, s[44:45]
	s_waitcnt vmcnt(36)
	v_pk_mul_f32 v[64:65], v[64:65], s[42:43] op_sel_hi:[1,0]
	v_pk_mul_f32 v[66:67], v[66:67], s[42:43] op_sel_hi:[1,0]
	v_pk_mul_f32 v[68:69], v[68:69], s[42:43] op_sel_hi:[1,0]
	v_pk_mul_f32 v[70:71], v[70:71], s[42:43] op_sel_hi:[1,0]
	v_pk_mul_f32 v[72:73], v[72:73], s[42:43] op_sel_hi:[1,0]
	v_pk_mul_f32 v[74:75], v[74:75], s[42:43] op_sel_hi:[1,0]
	v_pk_mul_f32 v[76:77], v[76:77], s[42:43] op_sel_hi:[1,0]
	v_pk_mul_f32 v[78:79], v[78:79], s[42:43] op_sel_hi:[1,0]
	v_pk_mul_f32 v[80:81], v[80:81], s[42:43] op_sel_hi:[1,0]
	v_pk_mul_f32 v[82:83], v[82:83], s[42:43] op_sel_hi:[1,0]
	v_pk_mul_f32 v[84:85], v[84:85], s[42:43] op_sel_hi:[1,0]
	v_pk_mul_f32 v[86:87], v[86:87], s[42:43] op_sel_hi:[1,0]
	v_pk_mul_f32 v[88:89], v[88:89], s[42:43] op_sel_hi:[1,0]
	v_pk_mul_f32 v[90:91], v[90:91], s[42:43] op_sel_hi:[1,0]
	v_pk_mul_f32 v[92:93], v[92:93], s[42:43] op_sel_hi:[1,0]
	v_pk_mul_f32 v[94:95], v[94:95], s[42:43] op_sel_hi:[1,0]
	v_pk_mul_f32 v[96:97], v[96:97], s[42:43] op_sel_hi:[1,0]
	v_pk_mul_f32 v[98:99], v[98:99], s[42:43] op_sel_hi:[1,0]
	v_pk_mul_f32 v[100:101], v[100:101], s[42:43] op_sel_hi:[1,0]
	v_pk_mul_f32 v[102:103], v[102:103], s[42:43] op_sel_hi:[1,0]
	v_pk_mul_f32 v[104:105], v[104:105], s[42:43] op_sel_hi:[1,0]
	v_pk_mul_f32 v[106:107], v[106:107], s[42:43] op_sel_hi:[1,0]
	v_pk_mul_f32 v[108:109], v[108:109], s[42:43] op_sel_hi:[1,0]
	v_pk_mul_f32 v[110:111], v[110:111], s[42:43] op_sel_hi:[1,0]
	v_pk_mul_f32 v[112:113], v[112:113], s[42:43] op_sel_hi:[1,0]
	v_pk_mul_f32 v[114:115], v[114:115], s[42:43] op_sel_hi:[1,0]
	v_pk_mul_f32 v[116:117], v[116:117], s[42:43] op_sel_hi:[1,0]
	v_pk_mul_f32 v[118:119], v[118:119], s[42:43] op_sel_hi:[1,0]
	v_pk_mul_f32 v[120:121], v[120:121], s[42:43] op_sel_hi:[1,0]
	v_pk_mul_f32 v[122:123], v[122:123], s[42:43] op_sel_hi:[1,0]
	v_pk_mul_f32 v[124:125], v[124:125], s[42:43] op_sel_hi:[1,0]
	v_pk_mul_f32 v[126:127], v[126:127], s[42:43] op_sel_hi:[1,0]
	v_cvt_pk_fp8_f32 v144, v64, v66
	v_cvt_pk_fp8_f32 v145, v72, v74
	v_cvt_pk_fp8_f32 v146, v80, v82
	v_cvt_pk_fp8_f32 v147, v88, v90
	v_cvt_pk_fp8_f32 v148, v96, v98
	v_cvt_pk_fp8_f32 v149, v104, v106
	v_cvt_pk_fp8_f32 v150, v112, v114
	v_cvt_pk_fp8_f32 v151, v120, v122
	v_cvt_pk_fp8_f32 v144, v68, v70 op_sel:[0,0,1]
	v_cvt_pk_fp8_f32 v145, v76, v78 op_sel:[0,0,1]
	v_cvt_pk_fp8_f32 v146, v84, v86 op_sel:[0,0,1]
	v_cvt_pk_fp8_f32 v147, v92, v94 op_sel:[0,0,1]
	v_cvt_pk_fp8_f32 v148, v100, v102 op_sel:[0,0,1]
	v_cvt_pk_fp8_f32 v149, v108, v110 op_sel:[0,0,1]
	v_cvt_pk_fp8_f32 v150, v116, v118 op_sel:[0,0,1]
	v_cvt_pk_fp8_f32 v151, v124, v126 op_sel:[0,0,1]
	v_cvt_pk_fp8_f32 v152, v65, v67
	v_cvt_pk_fp8_f32 v153, v73, v75
	v_cvt_pk_fp8_f32 v154, v81, v83
	v_cvt_pk_fp8_f32 v155, v89, v91
	v_cvt_pk_fp8_f32 v156, v97, v99
	v_cvt_pk_fp8_f32 v157, v105, v107
	v_cvt_pk_fp8_f32 v158, v113, v115
	v_cvt_pk_fp8_f32 v159, v121, v123
	v_cvt_pk_fp8_f32 v152, v69, v71 op_sel:[0,0,1]
	v_cvt_pk_fp8_f32 v153, v77, v79 op_sel:[0,0,1]
	v_cvt_pk_fp8_f32 v154, v85, v87 op_sel:[0,0,1]
	v_cvt_pk_fp8_f32 v155, v93, v95 op_sel:[0,0,1]
	v_cvt_pk_fp8_f32 v156, v101, v103 op_sel:[0,0,1]
	v_cvt_pk_fp8_f32 v157, v109, v111 op_sel:[0,0,1]
	v_cvt_pk_fp8_f32 v158, v117, v119 op_sel:[0,0,1]
	v_cvt_pk_fp8_f32 v159, v125, v127 op_sel:[0,0,1]
	s_nop 1
	global_store_dwordx4 v163, v[144:147], s[40:41]
	global_store_dwordx4 v163, v[148:151], s[40:41] offset:16
	global_store_dwordx4 v165, v[152:155], s[40:41]
	global_store_dwordx4 v165, v[156:159], s[40:41] offset:16
	s_sub_u32 s55, s101, 0x2200
	s_cmp_lt_u32 s55, 0x7000
	s_cbranch_scc0 .LfcA_dn_l1
; __device__ __forceinline__ void tr_item8(const float* W, int ld, int K, int nblk, int item, unsigned char* WT, bool gu, float scale, LAS float* scr, int lane) {
;     const int kb = item / nblk, nb = item % nblk, k0 = 64 * kb, n0 = 32 * nb;
;     int drow0 = n0;
;     if (gu) { const int bj = n0 / FF, j = n0 - bj * FF; drow0 = 256 * (j / 128) + 128 * bj + (j % 128); }
; __device__ __forceinline__ void convert_items(Frame& F, const Args& a, int lo, int hi, int w, int nw) {
;     ...
;         if (r < NE * I_GU) { const int e = r / I_GU, rr = r % I_GU; tr_item8(a.in[18] + (size_t)e * D * 2 * FF, 2 * FF, D, 224, rr, F.ws + WS_WMGU + (size_t)e * 2 * FF * D, true, WSC_GU, scr, lane); continue; } r -= NE * I_GU;
;         { const int e = r / I_DN, rr = r % I_DN; tr_item8(a.in[19] + (size_t)e * FF * D, D, FF, 32, rr, F.ws + WS_WMDN + (size_t)e * D * FF, false, WSC_DN, scr, lane); }
	s_lshr_b32 s54, s55, 9
	s_mulk_i32 s54, 0x2493
	s_lshr_b32 s54, s54, 16
	s_mul_i32 s53, s54, 0xe00
	s_sub_u32 s53, s55, s53
	s_lshr_b32 s52, s53, 5
	s_mulk_i32 s52, 0x2493
	s_lshr_b32 s52, s52, 16
	s_mul_i32 s51, s52, 0xe0
	s_sub_u32 s51, s53, s51
	s_mul_i32 s50, s54, 0x1c00000
	s_mul_i32 s49, s52, 0x1c0000
	s_add_u32 s50, s50, s49
	s_lshl_b32 s49, s51, 7
	s_add_u32 s50, s50, s49
	s_add_u32 s30, s0, s50
	s_addc_u32 s31, s1, 0
	s_cmp_ge_u32 s51, 0x70
	s_cselect_b32 s50, 1, 0
	s_mul_i32 s49, s50, 0x70
	s_sub_u32 s49, s51, s49
	s_lshr_b32 s48, s49, 2
	s_lshl_b32 s48, s48, 8
	s_lshl_b32 s50, s50, 7
	s_add_u32 s48, s48, s50
	s_and_b32 s49, s49, 3
	s_lshl_b32 s49, s49, 5
	s_add_u32 s48, s48, s49
	s_lshl_b32 s48, s48, 10
	s_mul_i32 s50, s54, 0x700000
	s_add_u32 s48, s48, s50
	s_lshl_b32 s50, s52, 6
	s_add_u32 s48, s48, s50
	s_add_u32 s40, s6, s48
	s_addc_u32 s41, s7, 0
	s_movk_i32 s98, 0x7000
	s_mov_b32 s42, 0x42800000
	v_mov_b32_e32 v161, v166
	v_mov_b32_e32 v163, v168
	v_add_u32_e32 v165, 0x400, v168
	s_branch .LfcA_set_l1

; __device__ __forceinline__ void tr_item8(const float* W, int ld, int K, int nblk, int item, unsigned char* WT, bool gu, float scale, LAS float* scr, int lane) {
;     ...
;     { float t_[32];
; #pragma unroll
;       for (int i = 0; i < 32; ++i) t_[i] = W[(size_t)(k0 + 2 * i + (lane >> 5)) * ld + n0 + (lane & 31)];
; #pragma unroll
;       for (int i = 0; i < 32; ++i) scr[(2 * i + (lane >> 5)) * 33 + (lane & 31)] = t_[i] * scale; }
.LfcA_set_l1:
	s_add_u32 s101, s101, 0x800
	s_mov_b64 s[44:45], s[30:31]
	global_load_dwordx2 v[64:65], v161, s[44:45]
	s_add_u32 s44, s44, s98
	s_addc_u32 s45, s45, 0
	global_load_dwordx2 v[66:67], v161, s[44:45]
	s_add_u32 s44, s44, s98
	s_addc_u32 s45, s45, 0
	global_load_dwordx2 v[68:69], v161, s[44:45]
	s_add_u32 s44, s44, s98
	s_addc_u32 s45, s45, 0
	global_load_dwordx2 v[70:71], v161, s[44:45]
	s_add_u32 s44, s44, s98
	s_addc_u32 s45, s45, 0
	global_load_dwordx2 v[72:73], v161, s[44:45]
	s_add_u32 s44, s44, s98
	s_addc_u32 s45, s45, 0
	global_load_dwordx2 v[74:75], v161, s[44:45]
	s_add_u32 s44, s44, s98
	s_addc_u32 s45, s45, 0
	global_load_dwordx2 v[76:77], v161, s[44:45]
	s_add_u32 s44, s44, s98
	s_addc_u32 s45, s45, 0
	global_load_dwordx2 v[78:79], v161, s[44:45]
	s_add_u32 s44, s44, s98
	s_addc_u32 s45, s45, 0
	global_load_dwordx2 v[80:81], v161, s[44:45]
	s_add_u32 s44, s44, s98
	s_addc_u32 s45, s45, 0
	global_load_dwordx2 v[82:83], v161, s[44:45]
	s_add_u32 s44, s44, s98
	s_addc_u32 s45, s45, 0
	global_load_dwordx2 v[84:85], v161, s[44:45]
	s_add_u32 s44, s44, s98
	s_addc_u32 s45, s45, 0
	global_load_dwordx2 v[86:87], v161, s[44:45]
	s_add_u32 s44, s44, s98
	s_addc_u32 s45, s45, 0
	global_load_dwordx2 v[88:89], v161, s[44:45]
	s_add_u32 s44, s44, s98
	s_addc_u32 s45, s45, 0
	global_load_dwordx2 v[90:91], v161, s[44:45]
	s_add_u32 s44, s44, s98
	s_addc_u32 s45, s45, 0
	global_load_dwordx2 v[92:93], v161, s[44:45]
	s_add_u32 s44, s44, s98
	s_addc_u32 s45, s45, 0
	global_load_dwordx2 v[94:95], v161, s[44:45]
	s_add_u32 s44, s44, s98
	s_addc_u32 s45, s45, 0
	global_load_dwordx2 v[96:97], v161, s[44:45]
	s_add_u32 s44, s44, s98
	s_addc_u32 s45, s45, 0
	global_load_dwordx2 v[98:99], v161, s[44:45]
	s_add_u32 s44, s44, s98
	s_addc_u32 s45, s45, 0
	global_load_dwordx2 v[100:101], v161, s[44:45]
	s_add_u32 s44, s44, s98
	s_addc_u32 s45, s45, 0
	global_load_dwordx2 v[102:103], v161, s[44:45]
	s_add_u32 s44, s44, s98
	s_addc_u32 s45, s45, 0
	global_load_dwordx2 v[104:105], v161, s[44:45]
	s_add_u32 s44, s44, s98
	s_addc_u32 s45, s45, 0
	global_load_dwordx2 v[106:107], v161, s[44:45]
	s_add_u32 s44, s44, s98
	s_addc_u32 s45, s45, 0
	global_load_dwordx2 v[108:109], v161, s[44:45]
	s_add_u32 s44, s44, s98
	s_addc_u32 s45, s45, 0
	global_load_dwordx2 v[110:111], v161, s[44:45]
	s_add_u32 s44, s44, s98
	s_addc_u32 s45, s45, 0
	global_load_dwordx2 v[112:113], v161, s[44:45]
	s_add_u32 s44, s44, s98
	s_addc_u32 s45, s45, 0
	global_load_dwordx2 v[114:115], v161, s[44:45]
	s_add_u32 s44, s44, s98
	s_addc_u32 s45, s45, 0
	global_load_dwordx2 v[116:117], v161, s[44:45]
	s_add_u32 s44, s44, s98
	s_addc_u32 s45, s45, 0
	global_load_dwordx2 v[118:119], v161, s[44:45]
	s_add_u32 s44, s44, s98
	s_addc_u32 s45, s45, 0
	global_load_dwordx2 v[120:121], v161, s[44:45]
	s_add_u32 s44, s44, s98
	s_addc_u32 s45, s45, 0
	global_load_dwordx2 v[122:123], v161, s[44:45]
	s_add_u32 s44, s44, s98
	s_addc_u32 s45, s45, 0
	global_load_dwordx2 v[124:125], v161, s[44:45]
	s_add_u32 s44, s44, s98
	s_addc_u32 s45, s45, 0
	global_load_dwordx2 v[126:127], v161, s[44:45]
	s_sub_u32 s100, s100, 2
	s_cmp_gt_u32 s100, 2
	s_cbranch_scc1 .LfcA_loop
; __device__ __forceinline__ unsigned cvt_pk4_fp8(float a, float b, float c, float d) { int w = 0; w = __builtin_amdgcn_cvt_pk_fp8_f32(a, b, w, false); w = __builtin_amdgcn_cvt_pk_fp8_f32(c, d, w, true); return (unsigned)w; }
; #define GAS __attribute__((address_space(1)))
; #define LAS __attribute__((address_space(3)))
; #define LDS_WAIT() asm volatile("s_waitcnt lgkmcnt(0)" ::: "memory")
; __device__ __forceinline__ void tr_item8(const float* W, int ld, int K, int nblk, int item, unsigned char* WT, bool gu, float scale, LAS float* scr, int lane) {
;     ...
; #pragma unroll
;       for (int i = 0; i < 32; ++i) scr[(2 * i + (lane >> 5)) * 33 + (lane & 31)] = t_[i] * scale; }
;     LDS_WAIT(); asm volatile("" ::: "memory");
;     const int c = lane & 3;
; #pragma unroll
;     for (int j = 0; j < 2; ++j) { const int n = (lane >> 2) + 16 * j; const LAS float* sp = scr + (16 * c) * 33 + n;
;         v4u o; o.x = pg8::cvt_pk4_fp8(sp[0 * 33], sp[1 * 33], sp[2 * 33], sp[3 * 33]); o.y = pg8::cvt_pk4_fp8(sp[4 * 33], sp[5 * 33], sp[6 * 33], sp[7 * 33]);
;         o.z = pg8::cvt_pk4_fp8(sp[8 * 33], sp[9 * 33], sp[10 * 33], sp[11 * 33]); o.w = pg8::cvt_pk4_fp8(sp[12 * 33], sp[13 * 33], sp[14 * 33], sp[15 * 33]);
;         *(GAS v4u*)(WT + (size_t)(drow0 + n) * K + k0 + 16 * c) = o; }
.LfcA_epi:
	s_waitcnt vmcnt(32)
	v_pk_mul_f32 v[0:1], v[0:1], s[16:17] op_sel_hi:[1,0]
	v_pk_mul_f32 v[2:3], v[2:3], s[16:17] op_sel_hi:[1,0]
	v_pk_mul_f32 v[4:5], v[4:5], s[16:17] op_sel_hi:[1,0]
	v_pk_mul_f32 v[6:7], v[6:7], s[16:17] op_sel_hi:[1,0]
	v_pk_mul_f32 v[8:9], v[8:9], s[16:17] op_sel_hi:[1,0]
	v_pk_mul_f32 v[10:11], v[10:11], s[16:17] op_sel_hi:[1,0]
	v_pk_mul_f32 v[12:13], v[12:13], s[16:17] op_sel_hi:[1,0]
	v_pk_mul_f32 v[14:15], v[14:15], s[16:17] op_sel_hi:[1,0]
	v_pk_mul_f32 v[16:17], v[16:17], s[16:17] op_sel_hi:[1,0]
	v_pk_mul_f32 v[18:19], v[18:19], s[16:17] op_sel_hi:[1,0]
	v_pk_mul_f32 v[20:21], v[20:21], s[16:17] op_sel_hi:[1,0]
	v_pk_mul_f32 v[22:23], v[22:23], s[16:17] op_sel_hi:[1,0]
	v_pk_mul_f32 v[24:25], v[24:25], s[16:17] op_sel_hi:[1,0]
	v_pk_mul_f32 v[26:27], v[26:27], s[16:17] op_sel_hi:[1,0]
	v_pk_mul_f32 v[28:29], v[28:29], s[16:17] op_sel_hi:[1,0]
	v_pk_mul_f32 v[30:31], v[30:31], s[16:17] op_sel_hi:[1,0]
	v_pk_mul_f32 v[32:33], v[32:33], s[16:17] op_sel_hi:[1,0]
	v_pk_mul_f32 v[34:35], v[34:35], s[16:17] op_sel_hi:[1,0]
	v_pk_mul_f32 v[36:37], v[36:37], s[16:17] op_sel_hi:[1,0]
	v_pk_mul_f32 v[38:39], v[38:39], s[16:17] op_sel_hi:[1,0]
	v_pk_mul_f32 v[40:41], v[40:41], s[16:17] op_sel_hi:[1,0]
	v_pk_mul_f32 v[42:43], v[42:43], s[16:17] op_sel_hi:[1,0]
	v_pk_mul_f32 v[44:45], v[44:45], s[16:17] op_sel_hi:[1,0]
	v_pk_mul_f32 v[46:47], v[46:47], s[16:17] op_sel_hi:[1,0]
	v_pk_mul_f32 v[48:49], v[48:49], s[16:17] op_sel_hi:[1,0]
	v_pk_mul_f32 v[50:51], v[50:51], s[16:17] op_sel_hi:[1,0]
	v_pk_mul_f32 v[52:53], v[52:53], s[16:17] op_sel_hi:[1,0]
	v_pk_mul_f32 v[54:55], v[54:55], s[16:17] op_sel_hi:[1,0]
	v_pk_mul_f32 v[56:57], v[56:57], s[16:17] op_sel_hi:[1,0]
	v_pk_mul_f32 v[58:59], v[58:59], s[16:17] op_sel_hi:[1,0]
	v_pk_mul_f32 v[60:61], v[60:61], s[16:17] op_sel_hi:[1,0]
	v_pk_mul_f32 v[62:63], v[62:63], s[16:17] op_sel_hi:[1,0]
	v_cvt_pk_fp8_f32 v128, v0, v2
	v_cvt_pk_fp8_f32 v129, v8, v10
	v_cvt_pk_fp8_f32 v130, v16, v18
	v_cvt_pk_fp8_f32 v131, v24, v26
	v_cvt_pk_fp8_f32 v132, v32, v34
	v_cvt_pk_fp8_f32 v133, v40, v42
	v_cvt_pk_fp8_f32 v134, v48, v50
	v_cvt_pk_fp8_f32 v135, v56, v58
	v_cvt_pk_fp8_f32 v128, v4, v6 op_sel:[0,0,1]
	v_cvt_pk_fp8_f32 v129, v12, v14 op_sel:[0,0,1]
	v_cvt_pk_fp8_f32 v130, v20, v22 op_sel:[0,0,1]
	v_cvt_pk_fp8_f32 v131, v28, v30 op_sel:[0,0,1]
	v_cvt_pk_fp8_f32 v132, v36, v38 op_sel:[0,0,1]
	v_cvt_pk_fp8_f32 v133, v44, v46 op_sel:[0,0,1]
	v_cvt_pk_fp8_f32 v134, v52, v54 op_sel:[0,0,1]
	v_cvt_pk_fp8_f32 v135, v60, v62 op_sel:[0,0,1]
	v_cvt_pk_fp8_f32 v136, v1, v3
	v_cvt_pk_fp8_f32 v137, v9, v11
	v_cvt_pk_fp8_f32 v138, v17, v19
	v_cvt_pk_fp8_f32 v139, v25, v27
	v_cvt_pk_fp8_f32 v140, v33, v35
	v_cvt_pk_fp8_f32 v141, v41, v43
	v_cvt_pk_fp8_f32 v142, v49, v51
	v_cvt_pk_fp8_f32 v143, v57, v59
	v_cvt_pk_fp8_f32 v136, v5, v7 op_sel:[0,0,1]
	v_cvt_pk_fp8_f32 v137, v13, v15 op_sel:[0,0,1]
	v_cvt_pk_fp8_f32 v138, v21, v23 op_sel:[0,0,1]
	v_cvt_pk_fp8_f32 v139, v29, v31 op_sel:[0,0,1]
	v_cvt_pk_fp8_f32 v140, v37, v39 op_sel:[0,0,1]
	v_cvt_pk_fp8_f32 v141, v45, v47 op_sel:[0,0,1]
	v_cvt_pk_fp8_f32 v142, v53, v55 op_sel:[0,0,1]
	v_cvt_pk_fp8_f32 v143, v61, v63 op_sel:[0,0,1]
	s_nop 1
	global_store_dwordx4 v162, v[128:131], s[14:15]
	global_store_dwordx4 v162, v[132:135], s[14:15] offset:16
	global_store_dwordx4 v164, v[136:139], s[14:15]
	global_store_dwordx4 v164, v[140:143], s[14:15] offset:16
	s_waitcnt vmcnt(4)
	v_pk_mul_f32 v[64:65], v[64:65], s[42:43] op_sel_hi:[1,0]
	v_pk_mul_f32 v[66:67], v[66:67], s[42:43] op_sel_hi:[1,0]
	v_pk_mul_f32 v[68:69], v[68:69], s[42:43] op_sel_hi:[1,0]
	v_pk_mul_f32 v[70:71], v[70:71], s[42:43] op_sel_hi:[1,0]
	v_pk_mul_f32 v[72:73], v[72:73], s[42:43] op_sel_hi:[1,0]
	v_pk_mul_f32 v[74:75], v[74:75], s[42:43] op_sel_hi:[1,0]
	v_pk_mul_f32 v[76:77], v[76:77], s[42:43] op_sel_hi:[1,0]
	v_pk_mul_f32 v[78:79], v[78:79], s[42:43] op_sel_hi:[1,0]
	v_pk_mul_f32 v[80:81], v[80:81], s[42:43] op_sel_hi:[1,0]
	v_pk_mul_f32 v[82:83], v[82:83], s[42:43] op_sel_hi:[1,0]
	v_pk_mul_f32 v[84:85], v[84:85], s[42:43] op_sel_hi:[1,0]
	v_pk_mul_f32 v[86:87], v[86:87], s[42:43] op_sel_hi:[1,0]
	v_pk_mul_f32 v[88:89], v[88:89], s[42:43] op_sel_hi:[1,0]
	v_pk_mul_f32 v[90:91], v[90:91], s[42:43] op_sel_hi:[1,0]
	v_pk_mul_f32 v[92:93], v[92:93], s[42:43] op_sel_hi:[1,0]
	v_pk_mul_f32 v[94:95], v[94:95], s[42:43] op_sel_hi:[1,0]
	v_pk_mul_f32 v[96:97], v[96:97], s[42:43] op_sel_hi:[1,0]
	v_pk_mul_f32 v[98:99], v[98:99], s[42:43] op_sel_hi:[1,0]
	v_pk_mul_f32 v[100:101], v[100:101], s[42:43] op_sel_hi:[1,0]
	v_pk_mul_f32 v[102:103], v[102:103], s[42:43] op_sel_hi:[1,0]
	v_pk_mul_f32 v[104:105], v[104:105], s[42:43] op_sel_hi:[1,0]
	v_pk_mul_f32 v[106:107], v[106:107], s[42:43] op_sel_hi:[1,0]
	v_pk_mul_f32 v[108:109], v[108:109], s[42:43] op_sel_hi:[1,0]
	v_pk_mul_f32 v[110:111], v[110:111], s[42:43] op_sel_hi:[1,0]
	v_pk_mul_f32 v[112:113], v[112:113], s[42:43] op_sel_hi:[1,0]
	v_pk_mul_f32 v[114:115], v[114:115], s[42:43] op_sel_hi:[1,0]
	v_pk_mul_f32 v[116:117], v[116:117], s[42:43] op_sel_hi:[1,0]
	v_pk_mul_f32 v[118:119], v[118:119], s[42:43] op_sel_hi:[1,0]
	v_pk_mul_f32 v[120:121], v[120:121], s[42:43] op_sel_hi:[1,0]
	v_pk_mul_f32 v[122:123], v[122:123], s[42:43] op_sel_hi:[1,0]
	v_pk_mul_f32 v[124:125], v[124:125], s[42:43] op_sel_hi:[1,0]
	v_pk_mul_f32 v[126:127], v[126:127], s[42:43] op_sel_hi:[1,0]
	v_cvt_pk_fp8_f32 v144, v64, v66
	v_cvt_pk_fp8_f32 v145, v72, v74
	v_cvt_pk_fp8_f32 v146, v80, v82
	v_cvt_pk_fp8_f32 v147, v88, v90
	v_cvt_pk_fp8_f32 v148, v96, v98
	v_cvt_pk_fp8_f32 v149, v104, v106
	v_cvt_pk_fp8_f32 v150, v112, v114
	v_cvt_pk_fp8_f32 v151, v120, v122
	v_cvt_pk_fp8_f32 v144, v68, v70 op_sel:[0,0,1]
	v_cvt_pk_fp8_f32 v145, v76, v78 op_sel:[0,0,1]
	v_cvt_pk_fp8_f32 v146, v84, v86 op_sel:[0,0,1]
	v_cvt_pk_fp8_f32 v147, v92, v94 op_sel:[0,0,1]
	v_cvt_pk_fp8_f32 v148, v100, v102 op_sel:[0,0,1]
	v_cvt_pk_fp8_f32 v149, v108, v110 op_sel:[0,0,1]
	v_cvt_pk_fp8_f32 v150, v116, v118 op_sel:[0,0,1]
	v_cvt_pk_fp8_f32 v151, v124, v126 op_sel:[0,0,1]
	v_cvt_pk_fp8_f32 v152, v65, v67
	v_cvt_pk_fp8_f32 v153, v73, v75
	v_cvt_pk_fp8_f32 v154, v81, v83
	v_cvt_pk_fp8_f32 v155, v89, v91
	v_cvt_pk_fp8_f32 v156, v97, v99
	v_cvt_pk_fp8_f32 v157, v105, v107
	v_cvt_pk_fp8_f32 v158, v113, v115
	v_cvt_pk_fp8_f32 v159, v121, v123
	v_cvt_pk_fp8_f32 v152, v69, v71 op_sel:[0,0,1]
	v_cvt_pk_fp8_f32 v153, v77, v79 op_sel:[0,0,1]
	v_cvt_pk_fp8_f32 v154, v85, v87 op_sel:[0,0,1]
	v_cvt_pk_fp8_f32 v155, v93, v95 op_sel:[0,0,1]
	v_cvt_pk_fp8_f32 v156, v101, v103 op_sel:[0,0,1]
	v_cvt_pk_fp8_f32 v157, v109, v111 op_sel:[0,0,1]
	v_cvt_pk_fp8_f32 v158, v117, v119 op_sel:[0,0,1]
	v_cvt_pk_fp8_f32 v159, v125, v127 op_sel:[0,0,1]
	s_nop 1
	global_store_dwordx4 v163, v[144:147], s[40:41]
	global_store_dwordx4 v163, v[148:151], s[40:41] offset:16
	global_store_dwordx4 v165, v[152:155], s[40:41]
	global_store_dwordx4 v165, v[156:159], s[40:41] offset:16
	s_branch .LBB0_1358

; __device__ __forceinline__ unsigned cvt_pk4_fp8(float a, float b, float c, float d) { int w = 0; w = __builtin_amdgcn_cvt_pk_fp8_f32(a, b, w, false); w = __builtin_amdgcn_cvt_pk_fp8_f32(c, d, w, true); return (unsigned)w; }
; #define GAS __attribute__((address_space(1)))
; #define LAS __attribute__((address_space(3)))
; #define LDS_WAIT() asm volatile("s_waitcnt lgkmcnt(0)" ::: "memory")
; __device__ __forceinline__ void tr_item8(const float* W, int ld, int K, int nblk, int item, unsigned char* WT, bool gu, float scale, LAS float* scr, int lane) {
;     const int kb = item / nblk, nb = item % nblk, k0 = 64 * kb, n0 = 32 * nb;
;     int drow0 = n0;
;     if (gu) { const int bj = n0 / FF, j = n0 - bj * FF; drow0 = 256 * (j / 128) + 128 * bj + (j % 128); }
;     { float t_[32];
; #pragma unroll
;       for (int i = 0; i < 32; ++i) t_[i] = W[(size_t)(k0 + 2 * i + (lane >> 5)) * ld + n0 + (lane & 31)];
; #pragma unroll
;       for (int i = 0; i < 32; ++i) scr[(2 * i + (lane >> 5)) * 33 + (lane & 31)] = t_[i] * scale; }
;     LDS_WAIT(); asm volatile("" ::: "memory");
;     const int c = lane & 3;
; #pragma unroll
;     for (int j = 0; j < 2; ++j) { const int n = (lane >> 2) + 16 * j; const LAS float* sp = scr + (16 * c) * 33 + n;
;         v4u o; o.x = pg8::cvt_pk4_fp8(sp[0 * 33], sp[1 * 33], sp[2 * 33], sp[3 * 33]); o.y = pg8::cvt_pk4_fp8(sp[4 * 33], sp[5 * 33], sp[6 * 33], sp[7 * 33]);
;         o.z = pg8::cvt_pk4_fp8(sp[8 * 33], sp[9 * 33], sp[10 * 33], sp[11 * 33]); o.w = pg8::cvt_pk4_fp8(sp[12 * 33], sp[13 * 33], sp[14 * 33], sp[15 * 33]);
;         *(GAS v4u*)(WT + (size_t)(drow0 + n) * K + k0 + 16 * c) = o; }
; __global__ void __launch_bounds__(NWAVES * 64, 2) mk_fwd(Args args) {
;     ...
;             if (att) { swa_phase((char*)lds + RING_OFF, QO, KB, VB, XN, args.in[11], args.in[13], (LAS float*)(F.lds + RING_OFF + 100 * 1024), run, 128, F.wave);
;                        convert_items(F, args, lo + NODD, CONV_NITEMS, w, 128 * NWAVES); }
.LBB0_1403:
	s_cmpk_gt_i32 s3, 0xfff
	s_barrier
	v_mbcnt_lo_u32_b32 v4, -1, 0
	v_mbcnt_hi_u32_b32 v4, -1, v4
	s_cbranch_scc1 .LBB0_1434
	s_lshl_b32 s90, s3, 1
	s_add_u32 s90, s90, 0xba00
	s_mov_b64 exec, -1
	v_readlane_b32 s0, v254, 32
	v_readlane_b32 s1, v254, 33
	v_readlane_b32 s4, v254, 34
	v_readlane_b32 s5, v254, 35
	s_add_u32 s6, s78, 0x2600000
	s_addc_u32 s7, s79, 0
	s_add_u32 s8, s78, 0x5e00000
	s_addc_u32 s9, s79, 0
	s_movk_i32 s101, 2
	v_mbcnt_lo_u32_b32 v170, -1, 0
	v_mbcnt_hi_u32_b32 v170, -1, v170
	v_and_b32_e32 v171, 31, v170
	v_lshrrev_b32_e32 v172, 5, v170
	v_lshlrev_b32_e32 v170, 3, v171
	s_mov_b32 s98, 0xe0000
	v_mul_lo_u32 v166, v172, s98
	v_add_u32_e32 v166, v166, v170
	v_lshlrev_b32_e32 v167, 17, v172
	v_add_u32_e32 v167, v167, v170
	v_lshlrev_b32_e32 v172, 5, v172
	v_lshl_add_u32 v168, v171, 11, v172
	s_movk_i32 s98, 0x1c00
	v_mul_lo_u32 v169, v171, s98
	v_add_u32_e32 v169, v169, v172
	s_sub_u32 s98, s90, 0x2200
	s_cmp_lt_u32 s98, 0x7000
	s_cbranch_scc0 .LfcB_dn_p0
	s_lshr_b32 s89, s98, 9
	s_mulk_i32 s89, 0x2493
	s_lshr_b32 s89, s89, 16
	s_mul_i32 s88, s89, 0xe00
	s_sub_u32 s88, s98, s88
	s_lshr_b32 s75, s88, 5
	s_mulk_i32 s75, 0x2493
	s_lshr_b32 s75, s75, 16
	s_mul_i32 s74, s75, 0xe0
	s_sub_u32 s74, s88, s74
	s_mul_i32 s73, s89, 0x1c00000
	s_mul_i32 s72, s75, 0x1c0000
	s_add_u32 s73, s73, s72
	s_lshl_b32 s72, s74, 7
	s_add_u32 s73, s73, s72
	s_add_u32 s10, s0, s73
	s_addc_u32 s11, s1, 0
	s_cmp_ge_u32 s74, 0x70
	s_cselect_b32 s73, 1, 0
	s_mul_i32 s72, s73, 0x70
	s_sub_u32 s72, s74, s72
	s_lshr_b32 s71, s72, 2
	s_lshl_b32 s71, s71, 8
	s_lshl_b32 s73, s73, 7
	s_add_u32 s71, s71, s73
	s_and_b32 s72, s72, 3
	s_lshl_b32 s72, s72, 5
	s_add_u32 s71, s71, s72
	s_lshl_b32 s71, s71, 10
	s_mul_i32 s73, s89, 0x700000
	s_add_u32 s71, s71, s73
	s_lshl_b32 s73, s75, 6
	s_add_u32 s71, s71, s73
	s_add_u32 s12, s6, s71
	s_addc_u32 s13, s7, 0
	s_movk_i32 s100, 0x7000
	s_mov_b32 s14, 0x42800000
	v_mov_b32_e32 v160, v166
	v_mov_b32_e32 v162, v168
	v_add_u32_e32 v164, 0x400, v168
	s_branch .LfcB_set_p0
.LfcB_dn_p0:
	s_sub_u32 s98, s98, 0x7000
	s_lshr_b32 s89, s98, 8
	s_mulk_i32 s89, 0x2493
	s_lshr_b32 s89, s89, 16
	s_mul_i32 s88, s89, 0x700
	s_sub_u32 s88, s98, s88
	s_lshr_b32 s75, s88, 5
	s_and_b32 s74, s88, 31
	s_mul_i32 s73, s89, 0xe00000
	s_lshl_b32 s72, s75, 18
	s_add_u32 s73, s73, s72
	s_lshl_b32 s72, s74, 7
	s_add_u32 s73, s73, s72
	s_add_u32 s10, s4, s73
	s_addc_u32 s11, s5, 0
	s_mul_i32 s73, s89, 0x380000
	s_mul_i32 s72, s74, 0x1c000
	s_add_u32 s73, s73, s72
	s_lshl_b32 s72, s75, 6
	s_add_u32 s73, s73, s72
	s_add_u32 s12, s8, s73
	s_addc_u32 s13, s9, 0
	s_movk_i32 s100, 0x1000
	s_mov_b32 s14, 0x43000000
	v_mov_b32_e32 v160, v167
	v_mov_b32_e32 v162, v169
	v_add_u32_e32 v164, 0xe00, v169
.LfcB_set_p0:
	s_add_u32 s90, s90, 0x800
	s_mov_b64 s[36:37], s[10:11]
	global_load_dwordx2 v[0:1], v160, s[36:37]
	s_add_u32 s36, s36, s100
	s_addc_u32 s37, s37, 0
	global_load_dwordx2 v[2:3], v160, s[36:37]
	s_add_u32 s36, s36, s100
	s_addc_u32 s37, s37, 0
	global_load_dwordx2 v[4:5], v160, s[36:37]
	s_add_u32 s36, s36, s100
	s_addc_u32 s37, s37, 0
	global_load_dwordx2 v[6:7], v160, s[36:37]
	s_add_u32 s36, s36, s100
	s_addc_u32 s37, s37, 0
	global_load_dwordx2 v[8:9], v160, s[36:37]
	s_add_u32 s36, s36, s100
	s_addc_u32 s37, s37, 0
	global_load_dwordx2 v[10:11], v160, s[36:37]
	s_add_u32 s36, s36, s100
	s_addc_u32 s37, s37, 0
	global_load_dwordx2 v[12:13], v160, s[36:37]
	s_add_u32 s36, s36, s100
	s_addc_u32 s37, s37, 0
	global_load_dwordx2 v[14:15], v160, s[36:37]
	s_add_u32 s36, s36, s100
	s_addc_u32 s37, s37, 0
	global_load_dwordx2 v[16:17], v160, s[36:37]
	s_add_u32 s36, s36, s100
	s_addc_u32 s37, s37, 0
	global_load_dwordx2 v[18:19], v160, s[36:37]
	s_add_u32 s36, s36, s100
	s_addc_u32 s37, s37, 0
	global_load_dwordx2 v[20:21], v160, s[36:37]
	s_add_u32 s36, s36, s100
	s_addc_u32 s37, s37, 0
	global_load_dwordx2 v[22:23], v160, s[36:37]
	s_add_u32 s36, s36, s100
	s_addc_u32 s37, s37, 0
	global_load_dwordx2 v[24:25], v160, s[36:37]
	s_add_u32 s36, s36, s100
	s_addc_u32 s37, s37, 0
	global_load_dwordx2 v[26:27], v160, s[36:37]
	s_add_u32 s36, s36, s100
	s_addc_u32 s37, s37, 0
	global_load_dwordx2 v[28:29], v160, s[36:37]
	s_add_u32 s36, s36, s100
	s_addc_u32 s37, s37, 0
	global_load_dwordx2 v[30:31], v160, s[36:37]
	s_add_u32 s36, s36, s100
	s_addc_u32 s37, s37, 0
	global_load_dwordx2 v[32:33], v160, s[36:37]
	s_add_u32 s36, s36, s100
	s_addc_u32 s37, s37, 0
	global_load_dwordx2 v[34:35], v160, s[36:37]
	s_add_u32 s36, s36, s100
	s_addc_u32 s37, s37, 0
	global_load_dwordx2 v[36:37], v160, s[36:37]
	s_add_u32 s36, s36, s100
	s_addc_u32 s37, s37, 0
	global_load_dwordx2 v[38:39], v160, s[36:37]
	s_add_u32 s36, s36, s100
	s_addc_u32 s37, s37, 0
	global_load_dwordx2 v[40:41], v160, s[36:37]
	s_add_u32 s36, s36, s100
	s_addc_u32 s37, s37, 0
	global_load_dwordx2 v[42:43], v160, s[36:37]
	s_add_u32 s36, s36, s100
	s_addc_u32 s37, s37, 0
	global_load_dwordx2 v[44:45], v160, s[36:37]
	s_add_u32 s36, s36, s100
	s_addc_u32 s37, s37, 0
	global_load_dwordx2 v[46:47], v160, s[36:37]
	s_add_u32 s36, s36, s100
	s_addc_u32 s37, s37, 0
	global_load_dwordx2 v[48:49], v160, s[36:37]
	s_add_u32 s36, s36, s100
	s_addc_u32 s37, s37, 0
	global_load_dwordx2 v[50:51], v160, s[36:37]
	s_add_u32 s36, s36, s100
	s_addc_u32 s37, s37, 0
	global_load_dwordx2 v[52:53], v160, s[36:37]
	s_add_u32 s36, s36, s100
	s_addc_u32 s37, s37, 0
	global_load_dwordx2 v[54:55], v160, s[36:37]
	s_add_u32 s36, s36, s100
	s_addc_u32 s37, s37, 0
	global_load_dwordx2 v[56:57], v160, s[36:37]
	s_add_u32 s36, s36, s100
	s_addc_u32 s37, s37, 0
	global_load_dwordx2 v[58:59], v160, s[36:37]
	s_add_u32 s36, s36, s100
	s_addc_u32 s37, s37, 0
	global_load_dwordx2 v[60:61], v160, s[36:37]
	s_add_u32 s36, s36, s100
	s_addc_u32 s37, s37, 0
	global_load_dwordx2 v[62:63], v160, s[36:37]
	s_sub_u32 s98, s90, 0x2200
	s_cmp_lt_u32 s98, 0x7000
	s_cbranch_scc0 .LfcB_dn_p1
	s_lshr_b32 s89, s98, 9
	s_mulk_i32 s89, 0x2493
	s_lshr_b32 s89, s89, 16
	s_mul_i32 s88, s89, 0xe00
	s_sub_u32 s88, s98, s88
	s_lshr_b32 s75, s88, 5
	s_mulk_i32 s75, 0x2493
	s_lshr_b32 s75, s75, 16
	s_mul_i32 s74, s75, 0xe0
	s_sub_u32 s74, s88, s74
	s_mul_i32 s73, s89, 0x1c00000
	s_mul_i32 s72, s75, 0x1c0000
	s_add_u32 s73, s73, s72
	s_lshl_b32 s72, s74, 7
	s_add_u32 s73, s73, s72
	s_add_u32 s16, s0, s73
	s_addc_u32 s17, s1, 0
	s_cmp_ge_u32 s74, 0x70
	s_cselect_b32 s73, 1, 0
	s_mul_i32 s72, s73, 0x70
	s_sub_u32 s72, s74, s72
	s_lshr_b32 s71, s72, 2
	s_lshl_b32 s71, s71, 8
	s_lshl_b32 s73, s73, 7
	s_add_u32 s71, s71, s73
	s_and_b32 s72, s72, 3
	s_lshl_b32 s72, s72, 5
	s_add_u32 s71, s71, s72
	s_lshl_b32 s71, s71, 10
	s_mul_i32 s73, s89, 0x700000
	s_add_u32 s71, s71, s73
	s_lshl_b32 s73, s75, 6
	s_add_u32 s71, s71, s73
	s_add_u32 s26, s6, s71
	s_addc_u32 s27, s7, 0
	s_movk_i32 s99, 0x7000
	s_mov_b32 s30, 0x42800000
	v_mov_b32_e32 v161, v166
	v_mov_b32_e32 v163, v168
	v_add_u32_e32 v165, 0x400, v168
	s_branch .LfcB_set_p1
; #define LAS __attribute__((address_space(3)))
; __device__ __forceinline__ void tr_item8(const float* W, int ld, int K, int nblk, int item, unsigned char* WT, bool gu, float scale, LAS float* scr, int lane) {
;     const int kb = item / nblk, nb = item % nblk, k0 = 64 * kb, n0 = 32 * nb;
;     int drow0 = n0;
;     if (gu) { const int bj = n0 / FF, j = n0 - bj * FF; drow0 = 256 * (j / 128) + 128 * bj + (j % 128); }
;     { float t_[32];
; #pragma unroll
;       for (int i = 0; i < 32; ++i) t_[i] = W[(size_t)(k0 + 2 * i + (lane >> 5)) * ld + n0 + (lane & 31)];
; #pragma unroll
;       for (int i = 0; i < 32; ++i) scr[(2 * i + (lane >> 5)) * 33 + (lane & 31)] = t_[i] * scale; }
.LfcB_dn_p1:
	s_sub_u32 s98, s98, 0x7000
	s_lshr_b32 s89, s98, 8
	s_mulk_i32 s89, 0x2493
	s_lshr_b32 s89, s89, 16
	s_mul_i32 s88, s89, 0x700
	s_sub_u32 s88, s98, s88
	s_lshr_b32 s75, s88, 5
	s_and_b32 s74, s88, 31
	s_mul_i32 s73, s89, 0xe00000
	s_lshl_b32 s72, s75, 18
	s_add_u32 s73, s73, s72
	s_lshl_b32 s72, s74, 7
	s_add_u32 s73, s73, s72
	s_add_u32 s16, s4, s73
	s_addc_u32 s17, s5, 0
	s_mul_i32 s73, s89, 0x380000
	s_mul_i32 s72, s74, 0x1c000
	s_add_u32 s73, s73, s72
	s_lshl_b32 s72, s75, 6
	s_add_u32 s73, s73, s72
	s_add_u32 s26, s8, s73
	s_addc_u32 s27, s9, 0
	s_movk_i32 s99, 0x1000
	s_mov_b32 s30, 0x43000000
	v_mov_b32_e32 v161, v167
	v_mov_b32_e32 v163, v169
	v_add_u32_e32 v165, 0xe00, v169
.LfcB_set_p1:
	s_add_u32 s90, s90, 0x800
	s_mov_b64 s[36:37], s[16:17]
	global_load_dwordx2 v[64:65], v161, s[36:37]
	s_add_u32 s36, s36, s99
	s_addc_u32 s37, s37, 0
	global_load_dwordx2 v[66:67], v161, s[36:37]
	s_add_u32 s36, s36, s99
	s_addc_u32 s37, s37, 0
	global_load_dwordx2 v[68:69], v161, s[36:37]
	s_add_u32 s36, s36, s99
	s_addc_u32 s37, s37, 0
	global_load_dwordx2 v[70:71], v161, s[36:37]
	s_add_u32 s36, s36, s99
	s_addc_u32 s37, s37, 0
	global_load_dwordx2 v[72:73], v161, s[36:37]
	s_add_u32 s36, s36, s99
	s_addc_u32 s37, s37, 0
	global_load_dwordx2 v[74:75], v161, s[36:37]
	s_add_u32 s36, s36, s99
	s_addc_u32 s37, s37, 0
	global_load_dwordx2 v[76:77], v161, s[36:37]
	s_add_u32 s36, s36, s99
	s_addc_u32 s37, s37, 0
	global_load_dwordx2 v[78:79], v161, s[36:37]
	s_add_u32 s36, s36, s99
	s_addc_u32 s37, s37, 0
	global_load_dwordx2 v[80:81], v161, s[36:37]
	s_add_u32 s36, s36, s99
	s_addc_u32 s37, s37, 0
	global_load_dwordx2 v[82:83], v161, s[36:37]
	s_add_u32 s36, s36, s99
	s_addc_u32 s37, s37, 0
	global_load_dwordx2 v[84:85], v161, s[36:37]
	s_add_u32 s36, s36, s99
	s_addc_u32 s37, s37, 0
	global_load_dwordx2 v[86:87], v161, s[36:37]
	s_add_u32 s36, s36, s99
	s_addc_u32 s37, s37, 0
	global_load_dwordx2 v[88:89], v161, s[36:37]
	s_add_u32 s36, s36, s99
	s_addc_u32 s37, s37, 0
	global_load_dwordx2 v[90:91], v161, s[36:37]
	s_add_u32 s36, s36, s99
	s_addc_u32 s37, s37, 0
	global_load_dwordx2 v[92:93], v161, s[36:37]
	s_add_u32 s36, s36, s99
	s_addc_u32 s37, s37, 0
	global_load_dwordx2 v[94:95], v161, s[36:37]
	s_add_u32 s36, s36, s99
	s_addc_u32 s37, s37, 0
	global_load_dwordx2 v[96:97], v161, s[36:37]
	s_add_u32 s36, s36, s99
	s_addc_u32 s37, s37, 0
	global_load_dwordx2 v[98:99], v161, s[36:37]
	s_add_u32 s36, s36, s99
	s_addc_u32 s37, s37, 0
	global_load_dwordx2 v[100:101], v161, s[36:37]
	s_add_u32 s36, s36, s99
	s_addc_u32 s37, s37, 0
	global_load_dwordx2 v[102:103], v161, s[36:37]
	s_add_u32 s36, s36, s99
	s_addc_u32 s37, s37, 0
	global_load_dwordx2 v[104:105], v161, s[36:37]
	s_add_u32 s36, s36, s99
	s_addc_u32 s37, s37, 0
	global_load_dwordx2 v[106:107], v161, s[36:37]
	s_add_u32 s36, s36, s99
	s_addc_u32 s37, s37, 0
	global_load_dwordx2 v[108:109], v161, s[36:37]
	s_add_u32 s36, s36, s99
	s_addc_u32 s37, s37, 0
	global_load_dwordx2 v[110:111], v161, s[36:37]
	s_add_u32 s36, s36, s99
	s_addc_u32 s37, s37, 0
	global_load_dwordx2 v[112:113], v161, s[36:37]
	s_add_u32 s36, s36, s99
	s_addc_u32 s37, s37, 0
	global_load_dwordx2 v[114:115], v161, s[36:37]
	s_add_u32 s36, s36, s99
	s_addc_u32 s37, s37, 0
	global_load_dwordx2 v[116:117], v161, s[36:37]
	s_add_u32 s36, s36, s99
	s_addc_u32 s37, s37, 0
	global_load_dwordx2 v[118:119], v161, s[36:37]
	s_add_u32 s36, s36, s99
	s_addc_u32 s37, s37, 0
	global_load_dwordx2 v[120:121], v161, s[36:37]
	s_add_u32 s36, s36, s99
	s_addc_u32 s37, s37, 0
	global_load_dwordx2 v[122:123], v161, s[36:37]
	s_add_u32 s36, s36, s99
	s_addc_u32 s37, s37, 0
	global_load_dwordx2 v[124:125], v161, s[36:37]
	s_add_u32 s36, s36, s99
	s_addc_u32 s37, s37, 0
	global_load_dwordx2 v[126:127], v161, s[36:37]
	s_cmp_le_u32 s101, 2
	s_cbranch_scc1 .LfcB_epi
; __device__ __forceinline__ unsigned cvt_pk4_fp8(float a, float b, float c, float d) { int w = 0; w = __builtin_amdgcn_cvt_pk_fp8_f32(a, b, w, false); w = __builtin_amdgcn_cvt_pk_fp8_f32(c, d, w, true); return (unsigned)w; }
; #define GAS __attribute__((address_space(1)))
; #define LAS __attribute__((address_space(3)))
; #define LDS_WAIT() asm volatile("s_waitcnt lgkmcnt(0)" ::: "memory")
; __device__ __forceinline__ void tr_item8(const float* W, int ld, int K, int nblk, int item, unsigned char* WT, bool gu, float scale, LAS float* scr, int lane) {
;     ...
; #pragma unroll
;       for (int i = 0; i < 32; ++i) t_[i] = W[(size_t)(k0 + 2 * i + (lane >> 5)) * ld + n0 + (lane & 31)];
; #pragma unroll
;       for (int i = 0; i < 32; ++i) scr[(2 * i + (lane >> 5)) * 33 + (lane & 31)] = t_[i] * scale; }
;     LDS_WAIT(); asm volatile("" ::: "memory");
;     const int c = lane & 3;
; #pragma unroll
;     for (int j = 0; j < 2; ++j) { const int n = (lane >> 2) + 16 * j; const LAS float* sp = scr + (16 * c) * 33 + n;
;         v4u o; o.x = pg8::cvt_pk4_fp8(sp[0 * 33], sp[1 * 33], sp[2 * 33], sp[3 * 33]); o.y = pg8::cvt_pk4_fp8(sp[4 * 33], sp[5 * 33], sp[6 * 33], sp[7 * 33]);
;         o.z = pg8::cvt_pk4_fp8(sp[8 * 33], sp[9 * 33], sp[10 * 33], sp[11 * 33]); o.w = pg8::cvt_pk4_fp8(sp[12 * 33], sp[13 * 33], sp[14 * 33], sp[15 * 33]);
;         *(GAS v4u*)(WT + (size_t)(drow0 + n) * K + k0 + 16 * c) = o; }
.LfcB_loop:
	s_waitcnt vmcnt(32)
	v_pk_mul_f32 v[0:1], v[0:1], s[14:15] op_sel_hi:[1,0]
	v_pk_mul_f32 v[2:3], v[2:3], s[14:15] op_sel_hi:[1,0]
	v_pk_mul_f32 v[4:5], v[4:5], s[14:15] op_sel_hi:[1,0]
	v_pk_mul_f32 v[6:7], v[6:7], s[14:15] op_sel_hi:[1,0]
	v_pk_mul_f32 v[8:9], v[8:9], s[14:15] op_sel_hi:[1,0]
	v_pk_mul_f32 v[10:11], v[10:11], s[14:15] op_sel_hi:[1,0]
	v_pk_mul_f32 v[12:13], v[12:13], s[14:15] op_sel_hi:[1,0]
	v_pk_mul_f32 v[14:15], v[14:15], s[14:15] op_sel_hi:[1,0]
	v_pk_mul_f32 v[16:17], v[16:17], s[14:15] op_sel_hi:[1,0]
	v_pk_mul_f32 v[18:19], v[18:19], s[14:15] op_sel_hi:[1,0]
	v_pk_mul_f32 v[20:21], v[20:21], s[14:15] op_sel_hi:[1,0]
	v_pk_mul_f32 v[22:23], v[22:23], s[14:15] op_sel_hi:[1,0]
	v_pk_mul_f32 v[24:25], v[24:25], s[14:15] op_sel_hi:[1,0]
	v_pk_mul_f32 v[26:27], v[26:27], s[14:15] op_sel_hi:[1,0]
	v_pk_mul_f32 v[28:29], v[28:29], s[14:15] op_sel_hi:[1,0]
	v_pk_mul_f32 v[30:31], v[30:31], s[14:15] op_sel_hi:[1,0]
	v_pk_mul_f32 v[32:33], v[32:33], s[14:15] op_sel_hi:[1,0]
	v_pk_mul_f32 v[34:35], v[34:35], s[14:15] op_sel_hi:[1,0]
	v_pk_mul_f32 v[36:37], v[36:37], s[14:15] op_sel_hi:[1,0]
	v_pk_mul_f32 v[38:39], v[38:39], s[14:15] op_sel_hi:[1,0]
	v_pk_mul_f32 v[40:41], v[40:41], s[14:15] op_sel_hi:[1,0]
	v_pk_mul_f32 v[42:43], v[42:43], s[14:15] op_sel_hi:[1,0]
	v_pk_mul_f32 v[44:45], v[44:45], s[14:15] op_sel_hi:[1,0]
	v_pk_mul_f32 v[46:47], v[46:47], s[14:15] op_sel_hi:[1,0]
	v_pk_mul_f32 v[48:49], v[48:49], s[14:15] op_sel_hi:[1,0]
	v_pk_mul_f32 v[50:51], v[50:51], s[14:15] op_sel_hi:[1,0]
	v_pk_mul_f32 v[52:53], v[52:53], s[14:15] op_sel_hi:[1,0]
	v_pk_mul_f32 v[54:55], v[54:55], s[14:15] op_sel_hi:[1,0]
	v_pk_mul_f32 v[56:57], v[56:57], s[14:15] op_sel_hi:[1,0]
	v_pk_mul_f32 v[58:59], v[58:59], s[14:15] op_sel_hi:[1,0]
	v_pk_mul_f32 v[60:61], v[60:61], s[14:15] op_sel_hi:[1,0]
	v_pk_mul_f32 v[62:63], v[62:63], s[14:15] op_sel_hi:[1,0]
	v_cvt_pk_fp8_f32 v128, v0, v2
	v_cvt_pk_fp8_f32 v129, v8, v10
	v_cvt_pk_fp8_f32 v130, v16, v18
	v_cvt_pk_fp8_f32 v131, v24, v26
	v_cvt_pk_fp8_f32 v132, v32, v34
	v_cvt_pk_fp8_f32 v133, v40, v42
	v_cvt_pk_fp8_f32 v134, v48, v50
	v_cvt_pk_fp8_f32 v135, v56, v58
	v_cvt_pk_fp8_f32 v128, v4, v6 op_sel:[0,0,1]
	v_cvt_pk_fp8_f32 v129, v12, v14 op_sel:[0,0,1]
	v_cvt_pk_fp8_f32 v130, v20, v22 op_sel:[0,0,1]
	v_cvt_pk_fp8_f32 v131, v28, v30 op_sel:[0,0,1]
	v_cvt_pk_fp8_f32 v132, v36, v38 op_sel:[0,0,1]
	v_cvt_pk_fp8_f32 v133, v44, v46 op_sel:[0,0,1]
	v_cvt_pk_fp8_f32 v134, v52, v54 op_sel:[0,0,1]
	v_cvt_pk_fp8_f32 v135, v60, v62 op_sel:[0,0,1]
	v_cvt_pk_fp8_f32 v136, v1, v3
	v_cvt_pk_fp8_f32 v137, v9, v11
	v_cvt_pk_fp8_f32 v138, v17, v19
	v_cvt_pk_fp8_f32 v139, v25, v27
	v_cvt_pk_fp8_f32 v140, v33, v35
	v_cvt_pk_fp8_f32 v141, v41, v43
	v_cvt_pk_fp8_f32 v142, v49, v51
	v_cvt_pk_fp8_f32 v143, v57, v59
	v_cvt_pk_fp8_f32 v136, v5, v7 op_sel:[0,0,1]
	v_cvt_pk_fp8_f32 v137, v13, v15 op_sel:[0,0,1]
	v_cvt_pk_fp8_f32 v138, v21, v23 op_sel:[0,0,1]
	v_cvt_pk_fp8_f32 v139, v29, v31 op_sel:[0,0,1]
	v_cvt_pk_fp8_f32 v140, v37, v39 op_sel:[0,0,1]
	v_cvt_pk_fp8_f32 v141, v45, v47 op_sel:[0,0,1]
	v_cvt_pk_fp8_f32 v142, v53, v55 op_sel:[0,0,1]
	v_cvt_pk_fp8_f32 v143, v61, v63 op_sel:[0,0,1]
	s_nop 1
	global_store_dwordx4 v162, v[128:131], s[12:13]
	global_store_dwordx4 v162, v[132:135], s[12:13] offset:16
	global_store_dwordx4 v164, v[136:139], s[12:13]
	global_store_dwordx4 v164, v[140:143], s[12:13] offset:16
	s_sub_u32 s98, s90, 0x2200
	s_cmp_lt_u32 s98, 0x7000
	s_cbranch_scc0 .LfcB_dn_l0
	s_lshr_b32 s89, s98, 9
	s_mulk_i32 s89, 0x2493
	s_lshr_b32 s89, s89, 16
	s_mul_i32 s88, s89, 0xe00
	s_sub_u32 s88, s98, s88
	s_lshr_b32 s75, s88, 5
	s_mulk_i32 s75, 0x2493
	s_lshr_b32 s75, s75, 16
	s_mul_i32 s74, s75, 0xe0
	s_sub_u32 s74, s88, s74
	s_mul_i32 s73, s89, 0x1c00000
	s_mul_i32 s72, s75, 0x1c0000
	s_add_u32 s73, s73, s72
	s_lshl_b32 s72, s74, 7
	s_add_u32 s73, s73, s72
	s_add_u32 s10, s0, s73
	s_addc_u32 s11, s1, 0
	s_cmp_ge_u32 s74, 0x70
	s_cselect_b32 s73, 1, 0
	s_mul_i32 s72, s73, 0x70
	s_sub_u32 s72, s74, s72
	s_lshr_b32 s71, s72, 2
	s_lshl_b32 s71, s71, 8
	s_lshl_b32 s73, s73, 7
	s_add_u32 s71, s71, s73
	s_and_b32 s72, s72, 3
	s_lshl_b32 s72, s72, 5
	s_add_u32 s71, s71, s72
	s_lshl_b32 s71, s71, 10
	s_mul_i32 s73, s89, 0x700000
	s_add_u32 s71, s71, s73
	s_lshl_b32 s73, s75, 6
	s_add_u32 s71, s71, s73
	s_add_u32 s12, s6, s71
	s_addc_u32 s13, s7, 0
	s_movk_i32 s100, 0x7000
	s_mov_b32 s14, 0x42800000
	v_mov_b32_e32 v160, v166
	v_mov_b32_e32 v162, v168
	v_add_u32_e32 v164, 0x400, v168
	s_branch .LfcB_set_l0

; __device__ __forceinline__ unsigned cvt_pk4_fp8(float a, float b, float c, float d) { int w = 0; w = __builtin_amdgcn_cvt_pk_fp8_f32(a, b, w, false); w = __builtin_amdgcn_cvt_pk_fp8_f32(c, d, w, true); return (unsigned)w; }
; #define GAS __attribute__((address_space(1)))
; #define LAS __attribute__((address_space(3)))
; #define LDS_WAIT() asm volatile("s_waitcnt lgkmcnt(0)" ::: "memory")
; __device__ __forceinline__ void tr_item8(const float* W, int ld, int K, int nblk, int item, unsigned char* WT, bool gu, float scale, LAS float* scr, int lane) {
;     ...
;     { float t_[32];
; #pragma unroll
;       for (int i = 0; i < 32; ++i) t_[i] = W[(size_t)(k0 + 2 * i + (lane >> 5)) * ld + n0 + (lane & 31)];
; #pragma unroll
;       for (int i = 0; i < 32; ++i) scr[(2 * i + (lane >> 5)) * 33 + (lane & 31)] = t_[i] * scale; }
;     LDS_WAIT(); asm volatile("" ::: "memory");
;     const int c = lane & 3;
; #pragma unroll
;     for (int j = 0; j < 2; ++j) { const int n = (lane >> 2) + 16 * j; const LAS float* sp = scr + (16 * c) * 33 + n;
;         v4u o; o.x = pg8::cvt_pk4_fp8(sp[0 * 33], sp[1 * 33], sp[2 * 33], sp[3 * 33]); o.y = pg8::cvt_pk4_fp8(sp[4 * 33], sp[5 * 33], sp[6 * 33], sp[7 * 33]);
;         o.z = pg8::cvt_pk4_fp8(sp[8 * 33], sp[9 * 33], sp[10 * 33], sp[11 * 33]); o.w = pg8::cvt_pk4_fp8(sp[12 * 33], sp[13 * 33], sp[14 * 33], sp[15 * 33]);
;         *(GAS v4u*)(WT + (size_t)(drow0 + n) * K + k0 + 16 * c) = o; }
.LfcB_set_l0:
	s_add_u32 s90, s90, 0x800
	s_mov_b64 s[36:37], s[10:11]
	global_load_dwordx2 v[0:1], v160, s[36:37]
	s_add_u32 s36, s36, s100
	s_addc_u32 s37, s37, 0
	global_load_dwordx2 v[2:3], v160, s[36:37]
	s_add_u32 s36, s36, s100
	s_addc_u32 s37, s37, 0
	global_load_dwordx2 v[4:5], v160, s[36:37]
	s_add_u32 s36, s36, s100
	s_addc_u32 s37, s37, 0
	global_load_dwordx2 v[6:7], v160, s[36:37]
	s_add_u32 s36, s36, s100
	s_addc_u32 s37, s37, 0
	global_load_dwordx2 v[8:9], v160, s[36:37]
	s_add_u32 s36, s36, s100
	s_addc_u32 s37, s37, 0
	global_load_dwordx2 v[10:11], v160, s[36:37]
	s_add_u32 s36, s36, s100
	s_addc_u32 s37, s37, 0
	global_load_dwordx2 v[12:13], v160, s[36:37]
	s_add_u32 s36, s36, s100
	s_addc_u32 s37, s37, 0
	global_load_dwordx2 v[14:15], v160, s[36:37]
	s_add_u32 s36, s36, s100
	s_addc_u32 s37, s37, 0
	global_load_dwordx2 v[16:17], v160, s[36:37]
	s_add_u32 s36, s36, s100
	s_addc_u32 s37, s37, 0
	global_load_dwordx2 v[18:19], v160, s[36:37]
	s_add_u32 s36, s36, s100
	s_addc_u32 s37, s37, 0
	global_load_dwordx2 v[20:21], v160, s[36:37]
	s_add_u32 s36, s36, s100
	s_addc_u32 s37, s37, 0
	global_load_dwordx2 v[22:23], v160, s[36:37]
	s_add_u32 s36, s36, s100
	s_addc_u32 s37, s37, 0
	global_load_dwordx2 v[24:25], v160, s[36:37]
	s_add_u32 s36, s36, s100
	s_addc_u32 s37, s37, 0
	global_load_dwordx2 v[26:27], v160, s[36:37]
	s_add_u32 s36, s36, s100
	s_addc_u32 s37, s37, 0
	global_load_dwordx2 v[28:29], v160, s[36:37]
	s_add_u32 s36, s36, s100
	s_addc_u32 s37, s37, 0
	global_load_dwordx2 v[30:31], v160, s[36:37]
	s_add_u32 s36, s36, s100
	s_addc_u32 s37, s37, 0
	global_load_dwordx2 v[32:33], v160, s[36:37]
	s_add_u32 s36, s36, s100
	s_addc_u32 s37, s37, 0
	global_load_dwordx2 v[34:35], v160, s[36:37]
	s_add_u32 s36, s36, s100
	s_addc_u32 s37, s37, 0
	global_load_dwordx2 v[36:37], v160, s[36:37]
	s_add_u32 s36, s36, s100
	s_addc_u32 s37, s37, 0
	global_load_dwordx2 v[38:39], v160, s[36:37]
	s_add_u32 s36, s36, s100
	s_addc_u32 s37, s37, 0
	global_load_dwordx2 v[40:41], v160, s[36:37]
	s_add_u32 s36, s36, s100
	s_addc_u32 s37, s37, 0
	global_load_dwordx2 v[42:43], v160, s[36:37]
	s_add_u32 s36, s36, s100
	s_addc_u32 s37, s37, 0
	global_load_dwordx2 v[44:45], v160, s[36:37]
	s_add_u32 s36, s36, s100
	s_addc_u32 s37, s37, 0
	global_load_dwordx2 v[46:47], v160, s[36:37]
	s_add_u32 s36, s36, s100
	s_addc_u32 s37, s37, 0
	global_load_dwordx2 v[48:49], v160, s[36:37]
	s_add_u32 s36, s36, s100
	s_addc_u32 s37, s37, 0
	global_load_dwordx2 v[50:51], v160, s[36:37]
	s_add_u32 s36, s36, s100
	s_addc_u32 s37, s37, 0
	global_load_dwordx2 v[52:53], v160, s[36:37]
	s_add_u32 s36, s36, s100
	s_addc_u32 s37, s37, 0
	global_load_dwordx2 v[54:55], v160, s[36:37]
	s_add_u32 s36, s36, s100
	s_addc_u32 s37, s37, 0
	global_load_dwordx2 v[56:57], v160, s[36:37]
	s_add_u32 s36, s36, s100
	s_addc_u32 s37, s37, 0
	global_load_dwordx2 v[58:59], v160, s[36:37]
	s_add_u32 s36, s36, s100
	s_addc_u32 s37, s37, 0
	global_load_dwordx2 v[60:61], v160, s[36:37]
	s_add_u32 s36, s36, s100
	s_addc_u32 s37, s37, 0
	global_load_dwordx2 v[62:63], v160, s[36:37]
	s_waitcnt vmcnt(36)
	v_pk_mul_f32 v[64:65], v[64:65], s[30:31] op_sel_hi:[1,0]
	v_pk_mul_f32 v[66:67], v[66:67], s[30:31] op_sel_hi:[1,0]
	v_pk_mul_f32 v[68:69], v[68:69], s[30:31] op_sel_hi:[1,0]
	v_pk_mul_f32 v[70:71], v[70:71], s[30:31] op_sel_hi:[1,0]
	v_pk_mul_f32 v[72:73], v[72:73], s[30:31] op_sel_hi:[1,0]
	v_pk_mul_f32 v[74:75], v[74:75], s[30:31] op_sel_hi:[1,0]
	v_pk_mul_f32 v[76:77], v[76:77], s[30:31] op_sel_hi:[1,0]
	v_pk_mul_f32 v[78:79], v[78:79], s[30:31] op_sel_hi:[1,0]
	v_pk_mul_f32 v[80:81], v[80:81], s[30:31] op_sel_hi:[1,0]
	v_pk_mul_f32 v[82:83], v[82:83], s[30:31] op_sel_hi:[1,0]
	v_pk_mul_f32 v[84:85], v[84:85], s[30:31] op_sel_hi:[1,0]
	v_pk_mul_f32 v[86:87], v[86:87], s[30:31] op_sel_hi:[1,0]
	v_pk_mul_f32 v[88:89], v[88:89], s[30:31] op_sel_hi:[1,0]
	v_pk_mul_f32 v[90:91], v[90:91], s[30:31] op_sel_hi:[1,0]
	v_pk_mul_f32 v[92:93], v[92:93], s[30:31] op_sel_hi:[1,0]
	v_pk_mul_f32 v[94:95], v[94:95], s[30:31] op_sel_hi:[1,0]
	v_pk_mul_f32 v[96:97], v[96:97], s[30:31] op_sel_hi:[1,0]
	v_pk_mul_f32 v[98:99], v[98:99], s[30:31] op_sel_hi:[1,0]
	v_pk_mul_f32 v[100:101], v[100:101], s[30:31] op_sel_hi:[1,0]
	v_pk_mul_f32 v[102:103], v[102:103], s[30:31] op_sel_hi:[1,0]
	v_pk_mul_f32 v[104:105], v[104:105], s[30:31] op_sel_hi:[1,0]
	v_pk_mul_f32 v[106:107], v[106:107], s[30:31] op_sel_hi:[1,0]
	v_pk_mul_f32 v[108:109], v[108:109], s[30:31] op_sel_hi:[1,0]
	v_pk_mul_f32 v[110:111], v[110:111], s[30:31] op_sel_hi:[1,0]
	v_pk_mul_f32 v[112:113], v[112:113], s[30:31] op_sel_hi:[1,0]
	v_pk_mul_f32 v[114:115], v[114:115], s[30:31] op_sel_hi:[1,0]
	v_pk_mul_f32 v[116:117], v[116:117], s[30:31] op_sel_hi:[1,0]
	v_pk_mul_f32 v[118:119], v[118:119], s[30:31] op_sel_hi:[1,0]
	v_pk_mul_f32 v[120:121], v[120:121], s[30:31] op_sel_hi:[1,0]
	v_pk_mul_f32 v[122:123], v[122:123], s[30:31] op_sel_hi:[1,0]
	v_pk_mul_f32 v[124:125], v[124:125], s[30:31] op_sel_hi:[1,0]
	v_pk_mul_f32 v[126:127], v[126:127], s[30:31] op_sel_hi:[1,0]
	v_cvt_pk_fp8_f32 v144, v64, v66
	v_cvt_pk_fp8_f32 v145, v72, v74
	v_cvt_pk_fp8_f32 v146, v80, v82
	v_cvt_pk_fp8_f32 v147, v88, v90
	v_cvt_pk_fp8_f32 v148, v96, v98
	v_cvt_pk_fp8_f32 v149, v104, v106
	v_cvt_pk_fp8_f32 v150, v112, v114
	v_cvt_pk_fp8_f32 v151, v120, v122
	v_cvt_pk_fp8_f32 v144, v68, v70 op_sel:[0,0,1]
	v_cvt_pk_fp8_f32 v145, v76, v78 op_sel:[0,0,1]
	v_cvt_pk_fp8_f32 v146, v84, v86 op_sel:[0,0,1]
	v_cvt_pk_fp8_f32 v147, v92, v94 op_sel:[0,0,1]
	v_cvt_pk_fp8_f32 v148, v100, v102 op_sel:[0,0,1]
	v_cvt_pk_fp8_f32 v149, v108, v110 op_sel:[0,0,1]
	v_cvt_pk_fp8_f32 v150, v116, v118 op_sel:[0,0,1]
	v_cvt_pk_fp8_f32 v151, v124, v126 op_sel:[0,0,1]
	v_cvt_pk_fp8_f32 v152, v65, v67
	v_cvt_pk_fp8_f32 v153, v73, v75
	v_cvt_pk_fp8_f32 v154, v81, v83
	v_cvt_pk_fp8_f32 v155, v89, v91
	v_cvt_pk_fp8_f32 v156, v97, v99
	v_cvt_pk_fp8_f32 v157, v105, v107
	v_cvt_pk_fp8_f32 v158, v113, v115
	v_cvt_pk_fp8_f32 v159, v121, v123
	v_cvt_pk_fp8_f32 v152, v69, v71 op_sel:[0,0,1]
	v_cvt_pk_fp8_f32 v153, v77, v79 op_sel:[0,0,1]
	v_cvt_pk_fp8_f32 v154, v85, v87 op_sel:[0,0,1]
	v_cvt_pk_fp8_f32 v155, v93, v95 op_sel:[0,0,1]
	v_cvt_pk_fp8_f32 v156, v101, v103 op_sel:[0,0,1]
	v_cvt_pk_fp8_f32 v157, v109, v111 op_sel:[0,0,1]
	v_cvt_pk_fp8_f32 v158, v117, v119 op_sel:[0,0,1]
	v_cvt_pk_fp8_f32 v159, v125, v127 op_sel:[0,0,1]
	s_nop 1
	global_store_dwordx4 v163, v[144:147], s[26:27]
	global_store_dwordx4 v163, v[148:151], s[26:27] offset:16
	global_store_dwordx4 v165, v[152:155], s[26:27]
	global_store_dwordx4 v165, v[156:159], s[26:27] offset:16
	s_sub_u32 s98, s90, 0x2200
	s_cmp_lt_u32 s98, 0x7000
	s_cbranch_scc0 .LfcB_dn_l1
; __device__ __forceinline__ void tr_item8(const float* W, int ld, int K, int nblk, int item, unsigned char* WT, bool gu, float scale, LAS float* scr, int lane) {
;     const int kb = item / nblk, nb = item % nblk, k0 = 64 * kb, n0 = 32 * nb;
;     int drow0 = n0;
;     if (gu) { const int bj = n0 / FF, j = n0 - bj * FF; drow0 = 256 * (j / 128) + 128 * bj + (j % 128); }
; __device__ __forceinline__ void convert_items(Frame& F, const Args& a, int lo, int hi, int w, int nw) {
;     ...
;         if (r < NE * I_GU) { const int e = r / I_GU, rr = r % I_GU; tr_item8(a.in[18] + (size_t)e * D * 2 * FF, 2 * FF, D, 224, rr, F.ws + WS_WMGU + (size_t)e * 2 * FF * D, true, WSC_GU, scr, lane); continue; } r -= NE * I_GU;
;         { const int e = r / I_DN, rr = r % I_DN; tr_item8(a.in[19] + (size_t)e * FF * D, D, FF, 32, rr, F.ws + WS_WMDN + (size_t)e * D * FF, false, WSC_DN, scr, lane); }
	s_lshr_b32 s89, s98, 9
	s_mulk_i32 s89, 0x2493
	s_lshr_b32 s89, s89, 16
	s_mul_i32 s88, s89, 0xe00
	s_sub_u32 s88, s98, s88
	s_lshr_b32 s75, s88, 5
	s_mulk_i32 s75, 0x2493
	s_lshr_b32 s75, s75, 16
	s_mul_i32 s74, s75, 0xe0
	s_sub_u32 s74, s88, s74
	s_mul_i32 s73, s89, 0x1c00000
	s_mul_i32 s72, s75, 0x1c0000
	s_add_u32 s73, s73, s72
	s_lshl_b32 s72, s74, 7
	s_add_u32 s73, s73, s72
	s_add_u32 s16, s0, s73
	s_addc_u32 s17, s1, 0
	s_cmp_ge_u32 s74, 0x70
	s_cselect_b32 s73, 1, 0
	s_mul_i32 s72, s73, 0x70
	s_sub_u32 s72, s74, s72
	s_lshr_b32 s71, s72, 2
	s_lshl_b32 s71, s71, 8
	s_lshl_b32 s73, s73, 7
	s_add_u32 s71, s71, s73
	s_and_b32 s72, s72, 3
	s_lshl_b32 s72, s72, 5
	s_add_u32 s71, s71, s72
	s_lshl_b32 s71, s71, 10
	s_mul_i32 s73, s89, 0x700000
	s_add_u32 s71, s71, s73
	s_lshl_b32 s73, s75, 6
	s_add_u32 s71, s71, s73
	s_add_u32 s26, s6, s71
	s_addc_u32 s27, s7, 0
	s_movk_i32 s99, 0x7000
	s_mov_b32 s30, 0x42800000
	v_mov_b32_e32 v161, v166
	v_mov_b32_e32 v163, v168
	v_add_u32_e32 v165, 0x400, v168
	s_branch .LfcB_set_l1

; __device__ __forceinline__ void tr_item8(const float* W, int ld, int K, int nblk, int item, unsigned char* WT, bool gu, float scale, LAS float* scr, int lane) {
;     ...
;     { float t_[32];
; #pragma unroll
;       for (int i = 0; i < 32; ++i) t_[i] = W[(size_t)(k0 + 2 * i + (lane >> 5)) * ld + n0 + (lane & 31)];
; #pragma unroll
;       for (int i = 0; i < 32; ++i) scr[(2 * i + (lane >> 5)) * 33 + (lane & 31)] = t_[i] * scale; }
.LfcB_set_l1:
	s_add_u32 s90, s90, 0x800
	s_mov_b64 s[36:37], s[16:17]
	global_load_dwordx2 v[64:65], v161, s[36:37]
	s_add_u32 s36, s36, s99
	s_addc_u32 s37, s37, 0
	global_load_dwordx2 v[66:67], v161, s[36:37]
	s_add_u32 s36, s36, s99
	s_addc_u32 s37, s37, 0
	global_load_dwordx2 v[68:69], v161, s[36:37]
	s_add_u32 s36, s36, s99
	s_addc_u32 s37, s37, 0
	global_load_dwordx2 v[70:71], v161, s[36:37]
	s_add_u32 s36, s36, s99
	s_addc_u32 s37, s37, 0
	global_load_dwordx2 v[72:73], v161, s[36:37]
	s_add_u32 s36, s36, s99
	s_addc_u32 s37, s37, 0
	global_load_dwordx2 v[74:75], v161, s[36:37]
	s_add_u32 s36, s36, s99
	s_addc_u32 s37, s37, 0
	global_load_dwordx2 v[76:77], v161, s[36:37]
	s_add_u32 s36, s36, s99
	s_addc_u32 s37, s37, 0
	global_load_dwordx2 v[78:79], v161, s[36:37]
	s_add_u32 s36, s36, s99
	s_addc_u32 s37, s37, 0
	global_load_dwordx2 v[80:81], v161, s[36:37]
	s_add_u32 s36, s36, s99
	s_addc_u32 s37, s37, 0
	global_load_dwordx2 v[82:83], v161, s[36:37]
	s_add_u32 s36, s36, s99
	s_addc_u32 s37, s37, 0
	global_load_dwordx2 v[84:85], v161, s[36:37]
	s_add_u32 s36, s36, s99
	s_addc_u32 s37, s37, 0
	global_load_dwordx2 v[86:87], v161, s[36:37]
	s_add_u32 s36, s36, s99
	s_addc_u32 s37, s37, 0
	global_load_dwordx2 v[88:89], v161, s[36:37]
	s_add_u32 s36, s36, s99
	s_addc_u32 s37, s37, 0
	global_load_dwordx2 v[90:91], v161, s[36:37]
	s_add_u32 s36, s36, s99
	s_addc_u32 s37, s37, 0
	global_load_dwordx2 v[92:93], v161, s[36:37]
	s_add_u32 s36, s36, s99
	s_addc_u32 s37, s37, 0
	global_load_dwordx2 v[94:95], v161, s[36:37]
	s_add_u32 s36, s36, s99
	s_addc_u32 s37, s37, 0
	global_load_dwordx2 v[96:97], v161, s[36:37]
	s_add_u32 s36, s36, s99
	s_addc_u32 s37, s37, 0
	global_load_dwordx2 v[98:99], v161, s[36:37]
	s_add_u32 s36, s36, s99
	s_addc_u32 s37, s37, 0
	global_load_dwordx2 v[100:101], v161, s[36:37]
	s_add_u32 s36, s36, s99
	s_addc_u32 s37, s37, 0
	global_load_dwordx2 v[102:103], v161, s[36:37]
	s_add_u32 s36, s36, s99
	s_addc_u32 s37, s37, 0
	global_load_dwordx2 v[104:105], v161, s[36:37]
	s_add_u32 s36, s36, s99
	s_addc_u32 s37, s37, 0
	global_load_dwordx2 v[106:107], v161, s[36:37]
	s_add_u32 s36, s36, s99
	s_addc_u32 s37, s37, 0
	global_load_dwordx2 v[108:109], v161, s[36:37]
	s_add_u32 s36, s36, s99
	s_addc_u32 s37, s37, 0
	global_load_dwordx2 v[110:111], v161, s[36:37]
	s_add_u32 s36, s36, s99
	s_addc_u32 s37, s37, 0
	global_load_dwordx2 v[112:113], v161, s[36:37]
	s_add_u32 s36, s36, s99
	s_addc_u32 s37, s37, 0
	global_load_dwordx2 v[114:115], v161, s[36:37]
	s_add_u32 s36, s36, s99
	s_addc_u32 s37, s37, 0
	global_load_dwordx2 v[116:117], v161, s[36:37]
	s_add_u32 s36, s36, s99
	s_addc_u32 s37, s37, 0
	global_load_dwordx2 v[118:119], v161, s[36:37]
	s_add_u32 s36, s36, s99
	s_addc_u32 s37, s37, 0
	global_load_dwordx2 v[120:121], v161, s[36:37]
	s_add_u32 s36, s36, s99
	s_addc_u32 s37, s37, 0
	global_load_dwordx2 v[122:123], v161, s[36:37]
	s_add_u32 s36, s36, s99
	s_addc_u32 s37, s37, 0
	global_load_dwordx2 v[124:125], v161, s[36:37]
	s_add_u32 s36, s36, s99
	s_addc_u32 s37, s37, 0
	global_load_dwordx2 v[126:127], v161, s[36:37]
	s_sub_u32 s101, s101, 2
	s_cmp_gt_u32 s101, 2
	s_cbranch_scc1 .LfcB_loop
; __device__ __forceinline__ unsigned cvt_pk4_fp8(float a, float b, float c, float d) { int w = 0; w = __builtin_amdgcn_cvt_pk_fp8_f32(a, b, w, false); w = __builtin_amdgcn_cvt_pk_fp8_f32(c, d, w, true); return (unsigned)w; }
; #define GAS __attribute__((address_space(1)))
; #define LAS __attribute__((address_space(3)))
; #define LDS_WAIT() asm volatile("s_waitcnt lgkmcnt(0)" ::: "memory")
; __device__ __forceinline__ void tr_item8(const float* W, int ld, int K, int nblk, int item, unsigned char* WT, bool gu, float scale, LAS float* scr, int lane) {
;     ...
; #pragma unroll
;       for (int i = 0; i < 32; ++i) scr[(2 * i + (lane >> 5)) * 33 + (lane & 31)] = t_[i] * scale; }
;     LDS_WAIT(); asm volatile("" ::: "memory");
;     const int c = lane & 3;
; #pragma unroll
;     for (int j = 0; j < 2; ++j) { const int n = (lane >> 2) + 16 * j; const LAS float* sp = scr + (16 * c) * 33 + n;
;         v4u o; o.x = pg8::cvt_pk4_fp8(sp[0 * 33], sp[1 * 33], sp[2 * 33], sp[3 * 33]); o.y = pg8::cvt_pk4_fp8(sp[4 * 33], sp[5 * 33], sp[6 * 33], sp[7 * 33]);
;         o.z = pg8::cvt_pk4_fp8(sp[8 * 33], sp[9 * 33], sp[10 * 33], sp[11 * 33]); o.w = pg8::cvt_pk4_fp8(sp[12 * 33], sp[13 * 33], sp[14 * 33], sp[15 * 33]);
;         *(GAS v4u*)(WT + (size_t)(drow0 + n) * K + k0 + 16 * c) = o; }
.LfcB_epi:
	s_waitcnt vmcnt(32)
	v_pk_mul_f32 v[0:1], v[0:1], s[14:15] op_sel_hi:[1,0]
	v_pk_mul_f32 v[2:3], v[2:3], s[14:15] op_sel_hi:[1,0]
	v_pk_mul_f32 v[4:5], v[4:5], s[14:15] op_sel_hi:[1,0]
	v_pk_mul_f32 v[6:7], v[6:7], s[14:15] op_sel_hi:[1,0]
	v_pk_mul_f32 v[8:9], v[8:9], s[14:15] op_sel_hi:[1,0]
	v_pk_mul_f32 v[10:11], v[10:11], s[14:15] op_sel_hi:[1,0]
	v_pk_mul_f32 v[12:13], v[12:13], s[14:15] op_sel_hi:[1,0]
	v_pk_mul_f32 v[14:15], v[14:15], s[14:15] op_sel_hi:[1,0]
	v_pk_mul_f32 v[16:17], v[16:17], s[14:15] op_sel_hi:[1,0]
	v_pk_mul_f32 v[18:19], v[18:19], s[14:15] op_sel_hi:[1,0]
	v_pk_mul_f32 v[20:21], v[20:21], s[14:15] op_sel_hi:[1,0]
	v_pk_mul_f32 v[22:23], v[22:23], s[14:15] op_sel_hi:[1,0]
	v_pk_mul_f32 v[24:25], v[24:25], s[14:15] op_sel_hi:[1,0]
	v_pk_mul_f32 v[26:27], v[26:27], s[14:15] op_sel_hi:[1,0]
	v_pk_mul_f32 v[28:29], v[28:29], s[14:15] op_sel_hi:[1,0]
	v_pk_mul_f32 v[30:31], v[30:31], s[14:15] op_sel_hi:[1,0]
	v_pk_mul_f32 v[32:33], v[32:33], s[14:15] op_sel_hi:[1,0]
	v_pk_mul_f32 v[34:35], v[34:35], s[14:15] op_sel_hi:[1,0]
	v_pk_mul_f32 v[36:37], v[36:37], s[14:15] op_sel_hi:[1,0]
	v_pk_mul_f32 v[38:39], v[38:39], s[14:15] op_sel_hi:[1,0]
	v_pk_mul_f32 v[40:41], v[40:41], s[14:15] op_sel_hi:[1,0]
	v_pk_mul_f32 v[42:43], v[42:43], s[14:15] op_sel_hi:[1,0]
	v_pk_mul_f32 v[44:45], v[44:45], s[14:15] op_sel_hi:[1,0]
	v_pk_mul_f32 v[46:47], v[46:47], s[14:15] op_sel_hi:[1,0]
	v_pk_mul_f32 v[48:49], v[48:49], s[14:15] op_sel_hi:[1,0]
	v_pk_mul_f32 v[50:51], v[50:51], s[14:15] op_sel_hi:[1,0]
	v_pk_mul_f32 v[52:53], v[52:53], s[14:15] op_sel_hi:[1,0]
	v_pk_mul_f32 v[54:55], v[54:55], s[14:15] op_sel_hi:[1,0]
	v_pk_mul_f32 v[56:57], v[56:57], s[14:15] op_sel_hi:[1,0]
	v_pk_mul_f32 v[58:59], v[58:59], s[14:15] op_sel_hi:[1,0]
	v_pk_mul_f32 v[60:61], v[60:61], s[14:15] op_sel_hi:[1,0]
	v_pk_mul_f32 v[62:63], v[62:63], s[14:15] op_sel_hi:[1,0]
	v_cvt_pk_fp8_f32 v128, v0, v2
	v_cvt_pk_fp8_f32 v129, v8, v10
	v_cvt_pk_fp8_f32 v130, v16, v18
	v_cvt_pk_fp8_f32 v131, v24, v26
	v_cvt_pk_fp8_f32 v132, v32, v34
	v_cvt_pk_fp8_f32 v133, v40, v42
	v_cvt_pk_fp8_f32 v134, v48, v50
	v_cvt_pk_fp8_f32 v135, v56, v58
	v_cvt_pk_fp8_f32 v128, v4, v6 op_sel:[0,0,1]
	v_cvt_pk_fp8_f32 v129, v12, v14 op_sel:[0,0,1]
	v_cvt_pk_fp8_f32 v130, v20, v22 op_sel:[0,0,1]
	v_cvt_pk_fp8_f32 v131, v28, v30 op_sel:[0,0,1]
	v_cvt_pk_fp8_f32 v132, v36, v38 op_sel:[0,0,1]
	v_cvt_pk_fp8_f32 v133, v44, v46 op_sel:[0,0,1]
	v_cvt_pk_fp8_f32 v134, v52, v54 op_sel:[0,0,1]
	v_cvt_pk_fp8_f32 v135, v60, v62 op_sel:[0,0,1]
	v_cvt_pk_fp8_f32 v136, v1, v3
	v_cvt_pk_fp8_f32 v137, v9, v11
	v_cvt_pk_fp8_f32 v138, v17, v19
	v_cvt_pk_fp8_f32 v139, v25, v27
	v_cvt_pk_fp8_f32 v140, v33, v35
	v_cvt_pk_fp8_f32 v141, v41, v43
	v_cvt_pk_fp8_f32 v142, v49, v51
	v_cvt_pk_fp8_f32 v143, v57, v59
	v_cvt_pk_fp8_f32 v136, v5, v7 op_sel:[0,0,1]
	v_cvt_pk_fp8_f32 v137, v13, v15 op_sel:[0,0,1]
	v_cvt_pk_fp8_f32 v138, v21, v23 op_sel:[0,0,1]
	v_cvt_pk_fp8_f32 v139, v29, v31 op_sel:[0,0,1]
	v_cvt_pk_fp8_f32 v140, v37, v39 op_sel:[0,0,1]
	v_cvt_pk_fp8_f32 v141, v45, v47 op_sel:[0,0,1]
	v_cvt_pk_fp8_f32 v142, v53, v55 op_sel:[0,0,1]
	v_cvt_pk_fp8_f32 v143, v61, v63 op_sel:[0,0,1]
	s_nop 1
	global_store_dwordx4 v162, v[128:131], s[12:13]
	global_store_dwordx4 v162, v[132:135], s[12:13] offset:16
	global_store_dwordx4 v164, v[136:139], s[12:13]
	global_store_dwordx4 v164, v[140:143], s[12:13] offset:16
	s_waitcnt vmcnt(4)
	v_pk_mul_f32 v[64:65], v[64:65], s[30:31] op_sel_hi:[1,0]
	v_pk_mul_f32 v[66:67], v[66:67], s[30:31] op_sel_hi:[1,0]
	v_pk_mul_f32 v[68:69], v[68:69], s[30:31] op_sel_hi:[1,0]
	v_pk_mul_f32 v[70:71], v[70:71], s[30:31] op_sel_hi:[1,0]
	v_pk_mul_f32 v[72:73], v[72:73], s[30:31] op_sel_hi:[1,0]
	v_pk_mul_f32 v[74:75], v[74:75], s[30:31] op_sel_hi:[1,0]
	v_pk_mul_f32 v[76:77], v[76:77], s[30:31] op_sel_hi:[1,0]
	v_pk_mul_f32 v[78:79], v[78:79], s[30:31] op_sel_hi:[1,0]
	v_pk_mul_f32 v[80:81], v[80:81], s[30:31] op_sel_hi:[1,0]
	v_pk_mul_f32 v[82:83], v[82:83], s[30:31] op_sel_hi:[1,0]
	v_pk_mul_f32 v[84:85], v[84:85], s[30:31] op_sel_hi:[1,0]
	v_pk_mul_f32 v[86:87], v[86:87], s[30:31] op_sel_hi:[1,0]
	v_pk_mul_f32 v[88:89], v[88:89], s[30:31] op_sel_hi:[1,0]
	v_pk_mul_f32 v[90:91], v[90:91], s[30:31] op_sel_hi:[1,0]
	v_pk_mul_f32 v[92:93], v[92:93], s[30:31] op_sel_hi:[1,0]
	v_pk_mul_f32 v[94:95], v[94:95], s[30:31] op_sel_hi:[1,0]
	v_pk_mul_f32 v[96:97], v[96:97], s[30:31] op_sel_hi:[1,0]
	v_pk_mul_f32 v[98:99], v[98:99], s[30:31] op_sel_hi:[1,0]
	v_pk_mul_f32 v[100:101], v[100:101], s[30:31] op_sel_hi:[1,0]
	v_pk_mul_f32 v[102:103], v[102:103], s[30:31] op_sel_hi:[1,0]
	v_pk_mul_f32 v[104:105], v[104:105], s[30:31] op_sel_hi:[1,0]
	v_pk_mul_f32 v[106:107], v[106:107], s[30:31] op_sel_hi:[1,0]
	v_pk_mul_f32 v[108:109], v[108:109], s[30:31] op_sel_hi:[1,0]
	v_pk_mul_f32 v[110:111], v[110:111], s[30:31] op_sel_hi:[1,0]
	v_pk_mul_f32 v[112:113], v[112:113], s[30:31] op_sel_hi:[1,0]
	v_pk_mul_f32 v[114:115], v[114:115], s[30:31] op_sel_hi:[1,0]
	v_pk_mul_f32 v[116:117], v[116:117], s[30:31] op_sel_hi:[1,0]
	v_pk_mul_f32 v[118:119], v[118:119], s[30:31] op_sel_hi:[1,0]
	v_pk_mul_f32 v[120:121], v[120:121], s[30:31] op_sel_hi:[1,0]
	v_pk_mul_f32 v[122:123], v[122:123], s[30:31] op_sel_hi:[1,0]
	v_pk_mul_f32 v[124:125], v[124:125], s[30:31] op_sel_hi:[1,0]
	v_pk_mul_f32 v[126:127], v[126:127], s[30:31] op_sel_hi:[1,0]
	v_cvt_pk_fp8_f32 v144, v64, v66
	v_cvt_pk_fp8_f32 v145, v72, v74
	v_cvt_pk_fp8_f32 v146, v80, v82
	v_cvt_pk_fp8_f32 v147, v88, v90
	v_cvt_pk_fp8_f32 v148, v96, v98
	v_cvt_pk_fp8_f32 v149, v104, v106
	v_cvt_pk_fp8_f32 v150, v112, v114
	v_cvt_pk_fp8_f32 v151, v120, v122
	v_cvt_pk_fp8_f32 v144, v68, v70 op_sel:[0,0,1]
	v_cvt_pk_fp8_f32 v145, v76, v78 op_sel:[0,0,1]
	v_cvt_pk_fp8_f32 v146, v84, v86 op_sel:[0,0,1]
	v_cvt_pk_fp8_f32 v147, v92, v94 op_sel:[0,0,1]
	v_cvt_pk_fp8_f32 v148, v100, v102 op_sel:[0,0,1]
	v_cvt_pk_fp8_f32 v149, v108, v110 op_sel:[0,0,1]
	v_cvt_pk_fp8_f32 v150, v116, v118 op_sel:[0,0,1]
	v_cvt_pk_fp8_f32 v151, v124, v126 op_sel:[0,0,1]
	v_cvt_pk_fp8_f32 v152, v65, v67
	v_cvt_pk_fp8_f32 v153, v73, v75
	v_cvt_pk_fp8_f32 v154, v81, v83
	v_cvt_pk_fp8_f32 v155, v89, v91
	v_cvt_pk_fp8_f32 v156, v97, v99
	v_cvt_pk_fp8_f32 v157, v105, v107
	v_cvt_pk_fp8_f32 v158, v113, v115
	v_cvt_pk_fp8_f32 v159, v121, v123
	v_cvt_pk_fp8_f32 v152, v69, v71 op_sel:[0,0,1]
	v_cvt_pk_fp8_f32 v153, v77, v79 op_sel:[0,0,1]
	v_cvt_pk_fp8_f32 v154, v85, v87 op_sel:[0,0,1]
	v_cvt_pk_fp8_f32 v155, v93, v95 op_sel:[0,0,1]
	v_cvt_pk_fp8_f32 v156, v101, v103 op_sel:[0,0,1]
	v_cvt_pk_fp8_f32 v157, v109, v111 op_sel:[0,0,1]
	v_cvt_pk_fp8_f32 v158, v117, v119 op_sel:[0,0,1]
	v_cvt_pk_fp8_f32 v159, v125, v127 op_sel:[0,0,1]
	s_nop 1
	global_store_dwordx4 v163, v[144:147], s[26:27]
	global_store_dwordx4 v163, v[148:151], s[26:27] offset:16
	global_store_dwordx4 v165, v[152:155], s[26:27]
	global_store_dwordx4 v165, v[156:159], s[26:27] offset:16
	s_branch .LBB0_1434

; __device__ __forceinline__ int pg8_lane_id() { int l; asm volatile("v_mbcnt_lo_u32_b32 %0, -1, 0\n\tv_mbcnt_hi_u32_b32 %0, -1, %0" : "=v"(l)); return l; }
; #define LAS __attribute__((address_space(3)))
; __global__ void __launch_bounds__(NWAVES * 64, 2) mk_fwd(Args args) {
;     extern __shared__ __attribute__((aligned(16))) unsigned char lds[];
;     Frame F;
;     F.lds = (LAS unsigned char*)lds;
;     F.MISC = (volatile LAS unsigned*)(F.lds + MISC_OFF);
;     F.wave = __builtin_amdgcn_readfirstlane((int)threadIdx.x >> 6);
;     F.G = gridDim.x; { const int bx = blockIdx.x; F.vcu = (F.G % 8 == 0) ? (bx % 8) * (F.G / 8) + bx / 8 : bx; F.c = bx; F.loc = 0; }
;     F.ws = args.ws; F.ctl = (gu32*)(args.ws + WS_CTL);
;     for (int u = F.wave * 64 + pg8::pg8_lane_id(); u < (LDS_BYTES - LDSCTL_OFF) / 4; u += NWAVES * 64) ((LAS unsigned*)(F.lds + LDSCTL_OFF))[u] = 0u;
	.amdhsa_kernel _Z6mk_fwd4Args
		.amdhsa_group_segment_fixed_size 0
		.amdhsa_private_segment_fixed_size 0
		.amdhsa_kernarg_size 448
		.amdhsa_user_sgpr_count 2
		.amdhsa_user_sgpr_dispatch_ptr 0
		.amdhsa_user_sgpr_queue_ptr 0
		.amdhsa_user_sgpr_kernarg_segment_ptr 1
		.amdhsa_user_sgpr_dispatch_id 0
		.amdhsa_user_sgpr_kernarg_preload_length 0
		.amdhsa_user_sgpr_kernarg_preload_offset 0
		.amdhsa_user_sgpr_private_segment_size 0
		.amdhsa_uses_dynamic_stack 0
		.amdhsa_enable_private_segment 0
		.amdhsa_system_sgpr_workgroup_id_x 1
		.amdhsa_system_sgpr_workgroup_id_y 0
		.amdhsa_system_sgpr_workgroup_id_z 0
		.amdhsa_system_sgpr_workgroup_info 0
		.amdhsa_system_vgpr_workitem_id 0
		.amdhsa_next_free_vgpr 256
		.amdhsa_next_free_sgpr 102
		.amdhsa_accum_offset 256
		.amdhsa_reserve_vcc 1
		.amdhsa_float_round_mode_32 0
		.amdhsa_float_round_mode_16_64 0
		.amdhsa_float_denorm_mode_32 3
		.amdhsa_float_denorm_mode_16_64 3
		.amdhsa_dx10_clamp 1
		.amdhsa_ieee_mode 1
		.amdhsa_fp16_overflow 0
		.amdhsa_tg_split 0
		.amdhsa_exception_fp_ieee_invalid_op 0
		.amdhsa_exception_fp_denorm_src 0
		.amdhsa_exception_fp_ieee_div_zero 0
		.amdhsa_exception_fp_ieee_overflow 0
		.amdhsa_exception_fp_ieee_underflow 0
		.amdhsa_exception_fp_ieee_inexact 0
		.amdhsa_exception_int_div_zero 0
	.end_amdhsa_kernel

; __device__ __forceinline__ int pg8_lane_id() { int l; asm volatile("v_mbcnt_lo_u32_b32 %0, -1, 0\n\tv_mbcnt_hi_u32_b32 %0, -1, %0" : "=v"(l)); return l; }
; #define LAS __attribute__((address_space(3)))
; __global__ void __launch_bounds__(NWAVES * 64, 2) mk_fwd(Args args) {
;     extern __shared__ __attribute__((aligned(16))) unsigned char lds[];
;     Frame F;
;     F.lds = (LAS unsigned char*)lds;
;     F.MISC = (volatile LAS unsigned*)(F.lds + MISC_OFF);
;     F.wave = __builtin_amdgcn_readfirstlane((int)threadIdx.x >> 6);
;     F.G = gridDim.x; { const int bx = blockIdx.x; F.vcu = (F.G % 8 == 0) ? (bx % 8) * (F.G / 8) + bx / 8 : bx; F.c = bx; F.loc = 0; }
;     F.ws = args.ws; F.ctl = (gu32*)(args.ws + WS_CTL);
;     for (int u = F.wave * 64 + pg8::pg8_lane_id(); u < (LDS_BYTES - LDSCTL_OFF) / 4; u += NWAVES * 64) ((LAS unsigned*)(F.lds + LDSCTL_OFF))[u] = 0u;
amdhsa.kernels:
  - .agpr_count:     0
    .args:
      - .offset:         0
        .size:           192
        .value_kind:     by_value
      - .offset:         192
        .size:           4
        .value_kind:     hidden_block_count_x
      - .offset:         196
        .size:           4
        .value_kind:     hidden_block_count_y
      - .offset:         200
        .size:           4
        .value_kind:     hidden_block_count_z
      - .offset:         204
        .size:           2
        .value_kind:     hidden_group_size_x
      - .offset:         206
        .size:           2
        .value_kind:     hidden_group_size_y
      - .offset:         208
        .size:           2
        .value_kind:     hidden_group_size_z
      - .offset:         210
        .size:           2
        .value_kind:     hidden_remainder_x
      - .offset:         212
        .size:           2
        .value_kind:     hidden_remainder_y
      - .offset:         214
        .size:           2
        .value_kind:     hidden_remainder_z
      - .offset:         232
        .size:           8
        .value_kind:     hidden_global_offset_x
      - .offset:         240
        .size:           8
        .value_kind:     hidden_global_offset_y
      - .offset:         248
        .size:           8
        .value_kind:     hidden_global_offset_z
      - .offset:         256
        .size:           2
        .value_kind:     hidden_grid_dims
      - .offset:         312
        .size:           4
        .value_kind:     hidden_dynamic_lds_size
    .group_segment_fixed_size: 0
    .kernarg_segment_align: 8
    .kernarg_segment_size: 448
    .language:       OpenCL C
    .language_version:
      - 2
      - 0
    .max_flat_workgroup_size: 512
    .name:           _Z6mk_fwd4Args
    .private_segment_fixed_size: 0
    .sgpr_count:     108
    .sgpr_spill_count: 100
    .symbol:         _Z6mk_fwd4Args.kd
    .uniform_work_group_size: 1
    .uses_dynamic_stack: false
    .vgpr_count:     256
    .vgpr_spill_count: 0
    .wavefront_size: 64
